# v18 plus loop-counter SALU before the last load wait, first fragment reads ahead of the unit scheduler (P3/P5/P11/P12), leftover s_nop after LDS-DMA removed
# speedup vs baseline: 1.0039x; 1.0039x over previous
.LBB0_261:
	s_nop 2
	ds_read_b128 v[0:3], v219
	ds_read_b128 v[4:7], v219 offset:1024
	ds_read_b128 v[8:11], v219 offset:2048
	ds_read_b128 v[12:15], v219 offset:3072
	ds_read_b128 v[16:19], v220
	ds_read_b128 v[20:23], v220 offset:1024
	ds_read_b128 v[24:27], v220 offset:2048
	ds_read_b128 v[28:31], v220 offset:3072
	ds_read_b128 v[32:35], v221
	ds_read_b128 v[36:39], v221 offset:1024
	ds_read_b128 v[40:43], v221 offset:2048
	ds_read_b128 v[44:47], v221 offset:3072
	ds_read_b128 v[48:51], v221 offset:4096
	ds_read_b128 v[52:55], v221 offset:5120
	ds_read_b128 v[56:59], v221 offset:6144
	ds_read_b128 v[60:63], v221 offset:7168
	s_add_u32 s8, s46, 0x100
	s_addc_u32 s9, s47, 0
	s_cmp_eq_u32 s76, 12
	s_cselect_b32 s52, s11, s8
	s_cselect_b32 s53, s7, s9
	s_cselect_b32 s48, s41, s77
	s_cselect_b32 s49, s39, s80
	s_add_u32 s12, s52, 0x80
	s_addc_u32 s13, s53, 0
	s_add_u32 s50, s48, 0x80
	s_addc_u32 s51, s49, 0
	s_add_u32 s46, s46, 0x40080
	s_addc_u32 s47, s47, 0
	s_add_i32 m0, s59, 0xc000
	s_nop 0
	global_load_lds_dwordx4 v215, s[46:47]
	s_add_i32 m0, s59, 0xe000
	s_nop 0
	global_load_lds_dwordx4 v217, s[46:47]
	s_waitcnt vmcnt(8) lgkmcnt(0)
	s_barrier
	v_mfma_i32_16x16x64_i8 v[172:175], v[0:3], v[48:51], v[172:175]
	v_mfma_i32_16x16x64_i8 v[168:171], v[8:11], v[48:51], v[168:171]
	v_mfma_i32_16x16x64_i8 v[152:155], v[8:11], v[56:59], v[152:155]
	v_mfma_i32_16x16x64_i8 v[156:159], v[0:3], v[56:59], v[156:159]
	v_mfma_i32_16x16x64_i8 v[64:67], v[0:3], v[32:35], v[204:207]
	v_mfma_i32_16x16x64_i8 v[76:79], v[8:11], v[32:35], v[200:203]
	v_mfma_i32_16x16x64_i8 v[92:95], v[8:11], v[40:43], v[184:187]
	v_mfma_i32_16x16x64_i8 v[80:83], v[0:3], v[40:43], v[188:191]
	v_mfma_i32_16x16x64_i8 v[172:175], v[4:7], v[52:55], v[172:175]
	v_mfma_i32_16x16x64_i8 v[168:171], v[12:15], v[52:55], v[168:171]
	v_mfma_i32_16x16x64_i8 v[152:155], v[12:15], v[60:63], v[152:155]
	v_mfma_i32_16x16x64_i8 v[156:159], v[4:7], v[60:63], v[156:159]
	v_mfma_i32_16x16x64_i8 v[64:67], v[4:7], v[36:39], v[64:67]
	v_mfma_i32_16x16x64_i8 v[76:79], v[12:15], v[36:39], v[76:79]
	v_mfma_i32_16x16x64_i8 v[92:95], v[12:15], v[44:47], v[92:95]
	v_mfma_i32_16x16x64_i8 v[80:83], v[4:7], v[44:47], v[80:83]
	v_mfma_i32_16x16x64_i8 v[184:187], v[16:19], v[32:35], v[196:199]
	v_mfma_i32_16x16x64_i8 v[32:35], v[24:27], v[32:35], v[192:195]
	v_mfma_i32_16x16x64_i8 v[196:199], v[20:23], v[36:39], v[184:187]
	v_mfma_i32_16x16x64_i8 v[32:35], v[28:31], v[36:39], v[32:35]
	v_mfma_i32_16x16x64_i8 v[36:39], v[16:19], v[40:43], v[180:183]
	v_mfma_i32_16x16x64_i8 v[40:43], v[24:27], v[40:43], v[176:179]
	v_mfma_i32_16x16x64_i8 v[36:39], v[20:23], v[44:47], v[36:39]
	v_mfma_i32_16x16x64_i8 v[40:43], v[28:31], v[44:47], v[40:43]
	v_mfma_i32_16x16x64_i8 v[44:47], v[16:19], v[48:51], v[164:167]
	v_mfma_i32_16x16x64_i8 v[48:51], v[24:27], v[48:51], v[160:163]
	v_mfma_i32_16x16x64_i8 v[44:47], v[20:23], v[52:55], v[44:47]
	v_mfma_i32_16x16x64_i8 v[48:51], v[28:31], v[52:55], v[48:51]
	v_mfma_i32_16x16x64_i8 v[52:55], v[16:19], v[56:59], v[148:151]
	v_mfma_i32_16x16x64_i8 v[56:59], v[24:27], v[56:59], v[144:147]
	v_mfma_i32_16x16x64_i8 v[52:55], v[20:23], v[60:63], v[52:55]
	v_mfma_i32_16x16x64_i8 v[56:59], v[28:31], v[60:63], v[56:59]
	s_barrier
	ds_read_b128 v[60:63], v221 offset:16384
	ds_read_b128 v[144:147], v221 offset:17408
	ds_read_b128 v[148:151], v221 offset:18432
	ds_read_b128 v[160:163], v221 offset:19456
	ds_read_b128 v[164:167], v221 offset:20480
	ds_read_b128 v[176:179], v221 offset:21504
	ds_read_b128 v[180:183], v221 offset:22528
	ds_read_b128 v[184:187], v221 offset:23552
	s_add_i32 m0, s59, 0x10000
	s_nop 0
	global_load_lds_dwordx4 v216, s[48:49]
	s_add_i32 m0, s59, 0x12000
	s_nop 0
	global_load_lds_dwordx4 v218, s[48:49]
	s_add_u32 s46, s48, 0x40000
	s_addc_u32 s47, s49, 0
	s_add_i32 m0, s59, 0x14000
	s_nop 0
	global_load_lds_dwordx4 v216, s[46:47]
	s_add_i32 m0, s59, 0x16000
	s_nop 0
	global_load_lds_dwordx4 v218, s[46:47]
	s_add_i32 m0, s59, 0
	s_nop 0
	global_load_lds_dwordx4 v215, s[52:53]
	s_add_i32 m0, s59, 0x2000
	s_nop 0
	global_load_lds_dwordx4 v217, s[52:53]
	s_waitcnt vmcnt(8) lgkmcnt(0)
	s_barrier
	v_mfma_i32_16x16x64_i8 v[140:143], v[0:3], v[60:63], v[140:143]
	v_mfma_i32_16x16x64_i8 v[124:127], v[0:3], v[148:151], v[124:127]
	v_mfma_i32_16x16x64_i8 v[108:111], v[0:3], v[164:167], v[108:111]
	v_mfma_i32_16x16x64_i8 v[0:3], v[0:3], v[180:183], v[88:91]
	v_mfma_i32_16x16x64_i8 v[136:139], v[8:11], v[60:63], v[136:139]
	v_mfma_i32_16x16x64_i8 v[120:123], v[8:11], v[148:151], v[120:123]
	v_mfma_i32_16x16x64_i8 v[104:107], v[8:11], v[164:167], v[104:107]
	v_mfma_i32_16x16x64_i8 v[88:91], v[4:7], v[184:187], v[0:3]
	v_mfma_i32_16x16x64_i8 v[0:3], v[8:11], v[180:183], v[84:87]
	v_mfma_i32_16x16x64_i8 v[140:143], v[4:7], v[144:147], v[140:143]
	v_mfma_i32_16x16x64_i8 v[136:139], v[12:15], v[144:147], v[136:139]
	v_mfma_i32_16x16x64_i8 v[124:127], v[4:7], v[160:163], v[124:127]
	v_mfma_i32_16x16x64_i8 v[120:123], v[12:15], v[160:163], v[120:123]
	v_mfma_i32_16x16x64_i8 v[108:111], v[4:7], v[176:179], v[108:111]
	v_mfma_i32_16x16x64_i8 v[104:107], v[12:15], v[176:179], v[104:107]
	v_mfma_i32_16x16x64_i8 v[84:87], v[12:15], v[184:187], v[0:3]
	v_mfma_i32_16x16x64_i8 v[0:3], v[16:19], v[60:63], v[132:135]
	v_mfma_i32_16x16x64_i8 v[132:135], v[20:23], v[144:147], v[0:3]
	v_mfma_i32_16x16x64_i8 v[0:3], v[24:27], v[60:63], v[128:131]
	v_mfma_i32_16x16x64_i8 v[128:131], v[28:31], v[144:147], v[0:3]
	v_mfma_i32_16x16x64_i8 v[0:3], v[16:19], v[148:151], v[116:119]
	v_mfma_i32_16x16x64_i8 v[116:119], v[20:23], v[160:163], v[0:3]
	v_mfma_i32_16x16x64_i8 v[0:3], v[24:27], v[148:151], v[112:115]
	v_mfma_i32_16x16x64_i8 v[112:115], v[28:31], v[160:163], v[0:3]
	v_mfma_i32_16x16x64_i8 v[0:3], v[16:19], v[164:167], v[100:103]
	v_mfma_i32_16x16x64_i8 v[100:103], v[20:23], v[176:179], v[0:3]
	v_mfma_i32_16x16x64_i8 v[0:3], v[24:27], v[164:167], v[96:99]
	v_mfma_i32_16x16x64_i8 v[96:99], v[28:31], v[176:179], v[0:3]
	v_mfma_i32_16x16x64_i8 v[0:3], v[16:19], v[180:183], v[72:75]
	v_mfma_i32_16x16x64_i8 v[72:75], v[20:23], v[184:187], v[0:3]
	v_mfma_i32_16x16x64_i8 v[0:3], v[24:27], v[180:183], v[68:71]
	v_mfma_i32_16x16x64_i8 v[68:71], v[28:31], v[184:187], v[0:3]
	s_barrier
	ds_read_b128 v[16:19], v222
	ds_read_b128 v[8:11], v222 offset:1024
	ds_read_b128 v[4:7], v222 offset:2048
	s_nop 1
	ds_read_b128 v[0:3], v222 offset:3072
	ds_read_b128 v[28:31], v223
	ds_read_b128 v[24:27], v223 offset:1024
	ds_read_b128 v[20:23], v223 offset:2048
	ds_read_b128 v[12:15], v223 offset:3072
	ds_read_b128 v[60:63], v221 offset:32768
	ds_read_b128 v[144:147], v221 offset:33792
	ds_read_b128 v[148:151], v221 offset:34816
	ds_read_b128 v[160:163], v221 offset:35840
	ds_read_b128 v[208:211], v221 offset:36864
	ds_read_b128 v[224:227], v221 offset:37888
	ds_read_b128 v[228:231], v221 offset:38912
	ds_read_b128 v[232:235], v221 offset:39936
	s_add_u32 s46, s52, 0x40000
	s_addc_u32 s47, s53, 0
	s_add_i32 m0, s59, 0x4000
	s_nop 0
	global_load_lds_dwordx4 v215, s[46:47]
	s_add_i32 m0, s59, 0x6000
	s_nop 0
	global_load_lds_dwordx4 v217, s[46:47]
	s_waitcnt vmcnt(8) lgkmcnt(0)
	s_barrier
	v_mfma_i32_16x16x64_i8 v[64:67], v[16:19], v[60:63], v[64:67]
	v_mfma_i32_16x16x64_i8 v[204:207], v[8:11], v[144:147], v[64:67]
	v_mfma_i32_16x16x64_i8 v[64:67], v[4:7], v[60:63], v[76:79]
	v_mfma_i32_16x16x64_i8 v[200:203], v[0:3], v[144:147], v[64:67]
	v_mfma_i32_16x16x64_i8 v[64:67], v[16:19], v[148:151], v[80:83]
	v_mfma_i32_16x16x64_i8 v[188:191], v[8:11], v[160:163], v[64:67]
	v_mfma_i32_16x16x64_i8 v[64:67], v[4:7], v[148:151], v[92:95]
	v_mfma_i32_16x16x64_i8 v[184:187], v[0:3], v[160:163], v[64:67]
	v_mfma_i32_16x16x64_i8 v[64:67], v[16:19], v[208:211], v[172:175]
	v_mfma_i32_16x16x64_i8 v[172:175], v[8:11], v[224:227], v[64:67]
	v_mfma_i32_16x16x64_i8 v[64:67], v[4:7], v[208:211], v[168:171]
	v_mfma_i32_16x16x64_i8 v[168:171], v[0:3], v[224:227], v[64:67]
	v_mfma_i32_16x16x64_i8 v[64:67], v[16:19], v[228:231], v[156:159]
	v_mfma_i32_16x16x64_i8 v[156:159], v[8:11], v[232:235], v[64:67]
	v_mfma_i32_16x16x64_i8 v[64:67], v[4:7], v[228:231], v[152:155]
	v_mfma_i32_16x16x64_i8 v[152:155], v[0:3], v[232:235], v[64:67]
	v_mfma_i32_16x16x64_i8 v[32:35], v[20:23], v[60:63], v[32:35]
	v_mfma_i32_16x16x64_i8 v[192:195], v[12:15], v[144:147], v[32:35]
	v_mfma_i32_16x16x64_i8 v[32:35], v[28:31], v[148:151], v[36:39]
	v_mfma_i32_16x16x64_i8 v[180:183], v[24:27], v[160:163], v[32:35]
	v_mfma_i32_16x16x64_i8 v[32:35], v[20:23], v[148:151], v[40:43]
	v_mfma_i32_16x16x64_i8 v[176:179], v[12:15], v[160:163], v[32:35]
	v_mfma_i32_16x16x64_i8 v[32:35], v[28:31], v[208:211], v[44:47]
	v_mfma_i32_16x16x64_i8 v[164:167], v[24:27], v[224:227], v[32:35]
	v_mfma_i32_16x16x64_i8 v[32:35], v[20:23], v[208:211], v[48:51]
	v_mfma_i32_16x16x64_i8 v[160:163], v[12:15], v[224:227], v[32:35]
	v_mfma_i32_16x16x64_i8 v[32:35], v[28:31], v[228:231], v[52:55]
	v_mfma_i32_16x16x64_i8 v[64:67], v[28:31], v[60:63], v[196:199]
	v_mfma_i32_16x16x64_i8 v[148:151], v[24:27], v[232:235], v[32:35]
	v_mfma_i32_16x16x64_i8 v[32:35], v[20:23], v[228:231], v[56:59]
	v_mfma_i32_16x16x64_i8 v[196:199], v[24:27], v[144:147], v[64:67]
	v_mfma_i32_16x16x64_i8 v[144:147], v[12:15], v[232:235], v[32:35]
	s_barrier
	ds_read_b128 v[60:63], v221 offset:49152
	ds_read_b128 v[56:59], v221 offset:50176
	ds_read_b128 v[52:55], v221 offset:51200
	ds_read_b128 v[48:51], v221 offset:52224
	ds_read_b128 v[44:47], v221 offset:53248
	ds_read_b128 v[40:43], v221 offset:54272
	ds_read_b128 v[36:39], v221 offset:55296
	ds_read_b128 v[32:35], v221 offset:56320
	s_add_i32 m0, s59, 0x18000
	s_nop 0
	global_load_lds_dwordx4 v216, s[50:51]
	s_add_i32 m0, s59, 0x1a000
	s_nop 0
	global_load_lds_dwordx4 v218, s[50:51]
	s_add_u32 s46, s48, 0x40080
	s_addc_u32 s47, s49, 0
	s_add_i32 m0, s59, 0x1c000
	s_nop 0
	global_load_lds_dwordx4 v216, s[46:47]
	s_add_i32 m0, s59, 0x1e000
	s_nop 0
	global_load_lds_dwordx4 v218, s[46:47]
	s_add_i32 m0, s59, 0x8000
	s_nop 0
	global_load_lds_dwordx4 v215, s[12:13]
	s_add_i32 m0, s59, 0xa000
	s_nop 0
	global_load_lds_dwordx4 v217, s[12:13]
	s_add_i32 s76, s76, 2
	s_add_u32 s77, s77, 0x100
	s_addc_u32 s80, s80, 0
	s_cmp_gt_u32 s76, 13
	s_mov_b64 s[46:47], s[8:9]
	s_waitcnt vmcnt(8) lgkmcnt(0)
	s_barrier
	v_mfma_i32_16x16x64_i8 v[64:67], v[16:19], v[60:63], v[140:143]
	v_mfma_i32_16x16x64_i8 v[140:143], v[8:11], v[56:59], v[64:67]
	v_mfma_i32_16x16x64_i8 v[64:67], v[4:7], v[60:63], v[136:139]
	v_mfma_i32_16x16x64_i8 v[136:139], v[0:3], v[56:59], v[64:67]
	v_mfma_i32_16x16x64_i8 v[64:67], v[16:19], v[52:55], v[124:127]
	v_mfma_i32_16x16x64_i8 v[124:127], v[8:11], v[48:51], v[64:67]
	v_mfma_i32_16x16x64_i8 v[64:67], v[4:7], v[52:55], v[120:123]
	v_mfma_i32_16x16x64_i8 v[120:123], v[0:3], v[48:51], v[64:67]
	v_mfma_i32_16x16x64_i8 v[64:67], v[16:19], v[44:47], v[108:111]
	v_mfma_i32_16x16x64_i8 v[108:111], v[8:11], v[40:43], v[64:67]
	v_mfma_i32_16x16x64_i8 v[64:67], v[4:7], v[44:47], v[104:107]
	v_mfma_i32_16x16x64_i8 v[104:107], v[0:3], v[40:43], v[64:67]
	v_mfma_i32_16x16x64_i8 v[64:67], v[16:19], v[36:39], v[88:91]
	v_mfma_i32_16x16x64_i8 v[88:91], v[8:11], v[32:35], v[64:67]
	v_mfma_i32_16x16x64_i8 v[64:67], v[4:7], v[36:39], v[84:87]
	v_mfma_i32_16x16x64_i8 v[84:87], v[0:3], v[32:35], v[64:67]
	v_mfma_i32_16x16x64_i8 v[64:67], v[28:31], v[60:63], v[132:135]
	v_mfma_i32_16x16x64_i8 v[132:135], v[24:27], v[56:59], v[64:67]
	v_mfma_i32_16x16x64_i8 v[64:67], v[20:23], v[60:63], v[128:131]
	v_mfma_i32_16x16x64_i8 v[128:131], v[12:15], v[56:59], v[64:67]
	v_mfma_i32_16x16x64_i8 v[64:67], v[28:31], v[52:55], v[116:119]
	v_mfma_i32_16x16x64_i8 v[116:119], v[24:27], v[48:51], v[64:67]
	v_mfma_i32_16x16x64_i8 v[64:67], v[20:23], v[52:55], v[112:115]
	v_mfma_i32_16x16x64_i8 v[112:115], v[12:15], v[48:51], v[64:67]
	v_mfma_i32_16x16x64_i8 v[64:67], v[28:31], v[44:47], v[100:103]
	v_mfma_i32_16x16x64_i8 v[100:103], v[24:27], v[40:43], v[64:67]
	v_mfma_i32_16x16x64_i8 v[64:67], v[20:23], v[44:47], v[96:99]
	v_mfma_i32_16x16x64_i8 v[96:99], v[12:15], v[40:43], v[64:67]
	v_mfma_i32_16x16x64_i8 v[64:67], v[28:31], v[36:39], v[72:75]
	v_mfma_i32_16x16x64_i8 v[72:75], v[24:27], v[32:35], v[64:67]
	v_mfma_i32_16x16x64_i8 v[64:67], v[20:23], v[36:39], v[68:71]
	v_mfma_i32_16x16x64_i8 v[68:71], v[12:15], v[32:35], v[64:67]
	s_barrier
	s_cbranch_scc0 .LBB0_261
	s_and_b64 vcc, exec, s[28:29]
	s_cbranch_vccz .LBB0_264
	s_barrier

.LBB0_602:
	s_ashr_i32 s25, s24, 31
	s_lshl_b64 s[26:27], s[24:25], 20
	s_add_u32 s26, s44, s26
	s_addc_u32 s27, s45, s27
	s_and_b64 s[28:29], s[4:5], exec
	s_waitcnt lgkmcnt(0)
	s_cselect_b32 s7, s27, s35
	s_cselect_b32 s9, s26, s34
	s_ashr_i32 s23, s22, 31
	s_lshl_b64 s[28:29], s[22:23], 20
	s_add_u32 s28, s46, s28
	s_addc_u32 s29, s47, s29
	s_and_b64 s[36:37], s[4:5], exec
	s_cselect_b32 s23, s29, s31
	s_cselect_b32 s25, s28, s30
	s_add_u32 s36, s34, 0x100
	s_addc_u32 s37, s35, 0
	s_add_u32 s42, s30, 0x100
	s_addc_u32 s43, s31, 0
	s_add_u32 s38, s34, 0x180
	s_addc_u32 s39, s35, 0
	s_add_u32 s40, s30, 0x180
	s_addc_u32 s41, s31, 0
	s_add_u32 s60, s34, 0x80080
	s_addc_u32 s61, s35, 0
	s_add_i32 m0, s48, 0xc000
	s_nop 0
	global_load_lds_dwordx4 v213, s[60:61]
	s_add_i32 m0, s48, 0xe000
	s_nop 0
	global_load_lds_dwordx4 v214, s[60:61]
	s_waitcnt vmcnt(8) lgkmcnt(0)
	s_barrier
	v_mfma_f32_16x16x32_bf16 v[64:67], v[0:3], v[32:35], 0
	v_mfma_f32_16x16x32_bf16 v[68:71], v[8:11], v[32:35], 0
	v_mfma_f32_16x16x32_bf16 v[72:75], v[0:3], v[40:43], 0
	v_mfma_f32_16x16x32_bf16 v[76:79], v[8:11], v[40:43], 0
	v_mfma_f32_16x16x32_bf16 v[80:83], v[0:3], v[48:51], 0
	v_mfma_f32_16x16x32_bf16 v[84:87], v[8:11], v[48:51], 0
	v_mfma_f32_16x16x32_bf16 v[88:91], v[0:3], v[56:59], 0
	v_mfma_f32_16x16x32_bf16 v[64:67], v[4:7], v[36:39], v[64:67]
	v_mfma_f32_16x16x32_bf16 v[68:71], v[12:15], v[36:39], v[68:71]
	v_mfma_f32_16x16x32_bf16 v[72:75], v[4:7], v[44:47], v[72:75]
	v_mfma_f32_16x16x32_bf16 v[76:79], v[12:15], v[44:47], v[76:79]
	v_mfma_f32_16x16x32_bf16 v[80:83], v[4:7], v[52:55], v[80:83]
	v_mfma_f32_16x16x32_bf16 v[84:87], v[12:15], v[52:55], v[84:87]
	v_mfma_f32_16x16x32_bf16 v[96:99], v[4:7], v[60:63], v[88:91]
	v_mfma_f32_16x16x32_bf16 v[88:91], v[8:11], v[56:59], 0
	v_mfma_f32_16x16x32_bf16 v[100:103], v[12:15], v[60:63], v[88:91]
	v_mfma_f32_16x16x32_bf16 v[88:91], v[16:19], v[32:35], 0
	v_mfma_f32_16x16x32_bf16 v[32:35], v[24:27], v[32:35], 0
	v_mfma_f32_16x16x32_bf16 v[104:107], v[20:23], v[36:39], v[88:91]
	v_mfma_f32_16x16x32_bf16 v[32:35], v[28:31], v[36:39], v[32:35]
	v_mfma_f32_16x16x32_bf16 v[36:39], v[16:19], v[40:43], 0
	v_mfma_f32_16x16x32_bf16 v[40:43], v[24:27], v[40:43], 0
	v_mfma_f32_16x16x32_bf16 v[36:39], v[20:23], v[44:47], v[36:39]
	v_mfma_f32_16x16x32_bf16 v[40:43], v[28:31], v[44:47], v[40:43]
	v_mfma_f32_16x16x32_bf16 v[44:47], v[16:19], v[48:51], 0
	v_mfma_f32_16x16x32_bf16 v[48:51], v[24:27], v[48:51], 0
	v_mfma_f32_16x16x32_bf16 v[44:47], v[20:23], v[52:55], v[44:47]
	v_mfma_f32_16x16x32_bf16 v[48:51], v[28:31], v[52:55], v[48:51]
	v_mfma_f32_16x16x32_bf16 v[52:55], v[16:19], v[56:59], 0
	v_mfma_f32_16x16x32_bf16 v[56:59], v[24:27], v[56:59], 0
	v_mfma_f32_16x16x32_bf16 v[52:55], v[20:23], v[60:63], v[52:55]
	v_mfma_f32_16x16x32_bf16 v[56:59], v[28:31], v[60:63], v[56:59]
	s_barrier
	ds_read_b128 v[60:63], v219 offset:16384
	ds_read_b128 v[88:91], v219 offset:17408
	ds_read_b128 v[92:95], v219 offset:18432
	ds_read_b128 v[108:111], v219 offset:19456
	ds_read_b128 v[112:115], v219 offset:20480
	ds_read_b128 v[116:119], v219 offset:21504
	ds_read_b128 v[120:123], v219 offset:22528
	ds_read_b128 v[124:127], v219 offset:23552
	s_add_i32 m0, s48, 0x10000
	s_nop 0
	global_load_lds_dwordx4 v213, s[42:43]
	s_add_i32 m0, s48, 0x12000
	s_nop 0
	global_load_lds_dwordx4 v214, s[42:43]
	s_add_u32 s42, s30, 0x80100
	s_addc_u32 s43, s31, 0
	s_add_i32 m0, s48, 0x14000
	s_nop 0
	global_load_lds_dwordx4 v213, s[42:43]
	s_add_i32 m0, s48, 0x16000
	s_nop 0
	global_load_lds_dwordx4 v214, s[42:43]
	s_add_i32 m0, s48, 0
	s_nop 0
	global_load_lds_dwordx4 v213, s[36:37]
	s_add_i32 m0, s48, 0x2000
	s_nop 0
	global_load_lds_dwordx4 v214, s[36:37]
	s_waitcnt vmcnt(8) lgkmcnt(0)
	s_barrier
	v_mfma_f32_16x16x32_bf16 v[128:131], v[0:3], v[60:63], 0
	v_mfma_f32_16x16x32_bf16 v[132:135], v[4:7], v[88:91], v[128:131]
	v_mfma_f32_16x16x32_bf16 v[128:131], v[8:11], v[60:63], 0
	v_mfma_f32_16x16x32_bf16 v[140:143], v[12:15], v[88:91], v[128:131]
	v_mfma_f32_16x16x32_bf16 v[128:131], v[0:3], v[92:95], 0
	v_mfma_f32_16x16x32_bf16 v[148:151], v[4:7], v[108:111], v[128:131]
	v_mfma_f32_16x16x32_bf16 v[128:131], v[8:11], v[92:95], 0
	v_mfma_f32_16x16x32_bf16 v[156:159], v[12:15], v[108:111], v[128:131]
	v_mfma_f32_16x16x32_bf16 v[128:131], v[0:3], v[112:115], 0
	v_mfma_f32_16x16x32_bf16 v[0:3], v[0:3], v[120:123], 0
	v_mfma_f32_16x16x32_bf16 v[160:163], v[4:7], v[116:119], v[128:131]
	v_mfma_f32_16x16x32_bf16 v[0:3], v[4:7], v[124:127], v[0:3]
	v_mfma_f32_16x16x32_bf16 v[4:7], v[8:11], v[120:123], 0
	v_mfma_f32_16x16x32_bf16 v[128:131], v[8:11], v[112:115], 0
	v_mfma_f32_16x16x32_bf16 v[4:7], v[12:15], v[124:127], v[4:7]
	v_mfma_f32_16x16x32_bf16 v[164:167], v[12:15], v[116:119], v[128:131]
	v_mfma_f32_16x16x32_bf16 v[8:11], v[16:19], v[60:63], 0
	v_mfma_f32_16x16x32_bf16 v[168:171], v[20:23], v[88:91], v[8:11]
	v_mfma_f32_16x16x32_bf16 v[8:11], v[24:27], v[60:63], 0
	v_mfma_f32_16x16x32_bf16 v[172:175], v[28:31], v[88:91], v[8:11]
	v_mfma_f32_16x16x32_bf16 v[8:11], v[16:19], v[92:95], 0
	v_mfma_f32_16x16x32_bf16 v[176:179], v[20:23], v[108:111], v[8:11]
	v_mfma_f32_16x16x32_bf16 v[8:11], v[24:27], v[92:95], 0
	v_mfma_f32_16x16x32_bf16 v[108:111], v[28:31], v[108:111], v[8:11]
	v_mfma_f32_16x16x32_bf16 v[8:11], v[16:19], v[112:115], 0
	v_mfma_f32_16x16x32_bf16 v[180:183], v[20:23], v[116:119], v[8:11]
	v_mfma_f32_16x16x32_bf16 v[8:11], v[24:27], v[112:115], 0
	v_mfma_f32_16x16x32_bf16 v[116:119], v[28:31], v[116:119], v[8:11]
	v_mfma_f32_16x16x32_bf16 v[8:11], v[16:19], v[120:123], 0
	v_mfma_f32_16x16x32_bf16 v[184:187], v[20:23], v[124:127], v[8:11]
	v_mfma_f32_16x16x32_bf16 v[8:11], v[24:27], v[120:123], 0
	v_mfma_f32_16x16x32_bf16 v[124:127], v[28:31], v[124:127], v[8:11]
	s_barrier
	s_nop 4
	ds_read_b128 v[8:11], v220
	ds_read_b128 v[12:15], v220 offset:1024
	ds_read_b128 v[16:19], v220 offset:2048
	ds_read_b128 v[20:23], v220 offset:3072
	ds_read_b128 v[194:197], v221
	ds_read_b128 v[198:201], v221 offset:1024
	ds_read_b128 v[202:205], v221 offset:2048
	ds_read_b128 v[206:209], v221 offset:3072
	ds_read_b128 v[24:27], v219 offset:32768
	ds_read_b128 v[28:31], v219 offset:33792
	ds_read_b128 v[60:63], v219 offset:34816
	ds_read_b128 v[224:227], v219 offset:35840
	ds_read_b128 v[228:231], v219 offset:36864
	ds_read_b128 v[232:235], v219 offset:37888
	ds_read_b128 v[236:239], v219 offset:38912
	ds_read_b128 v[240:243], v219 offset:39936
	s_add_u32 s34, s34, 0x80100
	s_addc_u32 s35, s35, 0
	s_add_i32 m0, s48, 0x4000
	s_nop 0
	global_load_lds_dwordx4 v213, s[34:35]
	s_add_i32 m0, s48, 0x6000
	s_nop 0
	global_load_lds_dwordx4 v214, s[34:35]
	s_waitcnt vmcnt(8) lgkmcnt(0)
	s_barrier
	v_mfma_f32_16x16x32_bf16 v[64:67], v[8:11], v[24:27], v[64:67]
	v_mfma_f32_16x16x32_bf16 v[152:155], v[12:15], v[28:31], v[64:67]
	v_mfma_f32_16x16x32_bf16 v[64:67], v[16:19], v[24:27], v[68:71]
	v_mfma_f32_16x16x32_bf16 v[144:147], v[20:23], v[28:31], v[64:67]
	v_mfma_f32_16x16x32_bf16 v[64:67], v[8:11], v[60:63], v[72:75]
	v_mfma_f32_16x16x32_bf16 v[120:123], v[12:15], v[224:227], v[64:67]
	v_mfma_f32_16x16x32_bf16 v[64:67], v[16:19], v[60:63], v[76:79]
	v_mfma_f32_16x16x32_bf16 v[112:115], v[20:23], v[224:227], v[64:67]
	v_mfma_f32_16x16x32_bf16 v[64:67], v[8:11], v[228:231], v[80:83]
	v_mfma_f32_16x16x32_bf16 v[92:95], v[12:15], v[232:235], v[64:67]
	v_mfma_f32_16x16x32_bf16 v[64:67], v[16:19], v[228:231], v[84:87]
	v_mfma_f32_16x16x32_bf16 v[88:91], v[20:23], v[232:235], v[64:67]
	v_mfma_f32_16x16x32_bf16 v[64:67], v[8:11], v[236:239], v[96:99]
	v_mfma_f32_16x16x32_bf16 v[76:79], v[12:15], v[240:243], v[64:67]
	v_mfma_f32_16x16x32_bf16 v[64:67], v[16:19], v[236:239], v[100:103]
	v_mfma_f32_16x16x32_bf16 v[72:75], v[20:23], v[240:243], v[64:67]
	v_mfma_f32_16x16x32_bf16 v[64:67], v[194:197], v[24:27], v[104:107]
	v_mfma_f32_16x16x32_bf16 v[24:27], v[202:205], v[24:27], v[32:35]
	v_mfma_f32_16x16x32_bf16 v[128:131], v[206:209], v[28:31], v[24:27]
	v_mfma_f32_16x16x32_bf16 v[24:27], v[194:197], v[60:63], v[36:39]
	v_mfma_f32_16x16x32_bf16 v[104:107], v[198:201], v[224:227], v[24:27]
	v_mfma_f32_16x16x32_bf16 v[24:27], v[202:205], v[60:63], v[40:43]
	v_mfma_f32_16x16x32_bf16 v[96:99], v[206:209], v[224:227], v[24:27]
	v_mfma_f32_16x16x32_bf16 v[24:27], v[194:197], v[228:231], v[44:47]
	v_mfma_f32_16x16x32_bf16 v[84:87], v[198:201], v[232:235], v[24:27]
	v_mfma_f32_16x16x32_bf16 v[24:27], v[202:205], v[228:231], v[48:51]
	v_mfma_f32_16x16x32_bf16 v[80:83], v[206:209], v[232:235], v[24:27]
	v_mfma_f32_16x16x32_bf16 v[24:27], v[194:197], v[236:239], v[52:55]
	v_mfma_f32_16x16x32_bf16 v[68:71], v[198:201], v[240:243], v[24:27]
	v_mfma_f32_16x16x32_bf16 v[24:27], v[202:205], v[236:239], v[56:59]
	v_mfma_f32_16x16x32_bf16 v[136:139], v[198:201], v[28:31], v[64:67]
	v_mfma_f32_16x16x32_bf16 v[64:67], v[206:209], v[240:243], v[24:27]
	s_barrier
	ds_read_b128 v[32:35], v219 offset:49152
	ds_read_b128 v[36:39], v219 offset:50176
	ds_read_b128 v[100:103], v219 offset:51200
	ds_read_b128 v[224:227], v219 offset:52224
	ds_read_b128 v[228:231], v219 offset:53248
	ds_read_b128 v[232:235], v219 offset:54272
	ds_read_b128 v[236:239], v219 offset:55296
	ds_read_b128 v[240:243], v219 offset:56320
	s_add_i32 m0, s48, 0x18000
	s_nop 0
	global_load_lds_dwordx4 v213, s[40:41]
	s_add_i32 m0, s48, 0x1a000
	s_nop 0
	global_load_lds_dwordx4 v214, s[40:41]
	s_add_u32 s34, s30, 0x80180
	s_addc_u32 s35, s31, 0
	s_add_i32 m0, s48, 0x1c000
	s_nop 0
	global_load_lds_dwordx4 v213, s[34:35]
	s_add_i32 m0, s48, 0x1e000
	s_nop 0
	global_load_lds_dwordx4 v214, s[34:35]
	s_add_i32 m0, s48, 0x8000
	s_nop 0
	global_load_lds_dwordx4 v213, s[38:39]
	s_add_i32 m0, s48, 0xa000
	s_nop 0
	global_load_lds_dwordx4 v214, s[38:39]
	s_waitcnt vmcnt(8) lgkmcnt(0)
	s_barrier
	v_mfma_f32_16x16x32_bf16 v[24:27], v[8:11], v[32:35], v[132:135]
	v_mfma_f32_16x16x32_bf16 v[60:63], v[12:15], v[36:39], v[24:27]
	v_mfma_f32_16x16x32_bf16 v[24:27], v[16:19], v[32:35], v[140:143]
	v_mfma_f32_16x16x32_bf16 v[56:59], v[20:23], v[36:39], v[24:27]
	v_mfma_f32_16x16x32_bf16 v[24:27], v[8:11], v[100:103], v[148:151]
	v_mfma_f32_16x16x32_bf16 v[44:47], v[12:15], v[224:227], v[24:27]
	v_mfma_f32_16x16x32_bf16 v[24:27], v[16:19], v[100:103], v[156:159]
	v_mfma_f32_16x16x32_bf16 v[40:43], v[20:23], v[224:227], v[24:27]
	v_mfma_f32_16x16x32_bf16 v[24:27], v[8:11], v[228:231], v[160:163]
	v_mfma_f32_16x16x32_bf16 v[0:3], v[8:11], v[236:239], v[0:3]
	v_mfma_f32_16x16x32_bf16 v[28:31], v[12:15], v[232:235], v[24:27]
	v_mfma_f32_16x16x32_bf16 v[24:27], v[16:19], v[228:231], v[164:167]
	v_mfma_f32_16x16x32_bf16 v[12:15], v[12:15], v[240:243], v[0:3]
	v_mfma_f32_16x16x32_bf16 v[0:3], v[16:19], v[236:239], v[4:7]
	v_mfma_f32_16x16x32_bf16 v[24:27], v[20:23], v[232:235], v[24:27]
	v_mfma_f32_16x16x32_bf16 v[8:11], v[20:23], v[240:243], v[0:3]
	v_mfma_f32_16x16x32_bf16 v[0:3], v[194:197], v[32:35], v[168:171]
	v_mfma_f32_16x16x32_bf16 v[52:55], v[198:201], v[36:39], v[0:3]
	v_mfma_f32_16x16x32_bf16 v[0:3], v[202:205], v[32:35], v[172:175]
	v_mfma_f32_16x16x32_bf16 v[48:51], v[206:209], v[36:39], v[0:3]
	v_mfma_f32_16x16x32_bf16 v[0:3], v[194:197], v[100:103], v[176:179]
	v_mfma_f32_16x16x32_bf16 v[36:39], v[198:201], v[224:227], v[0:3]
	v_mfma_f32_16x16x32_bf16 v[0:3], v[202:205], v[100:103], v[108:111]
	v_mfma_f32_16x16x32_bf16 v[32:35], v[206:209], v[224:227], v[0:3]
	v_mfma_f32_16x16x32_bf16 v[0:3], v[194:197], v[228:231], v[180:183]
	v_mfma_f32_16x16x32_bf16 v[20:23], v[198:201], v[232:235], v[0:3]
	v_mfma_f32_16x16x32_bf16 v[0:3], v[202:205], v[228:231], v[116:119]
	v_mfma_f32_16x16x32_bf16 v[16:19], v[206:209], v[232:235], v[0:3]
	v_mfma_f32_16x16x32_bf16 v[0:3], v[194:197], v[236:239], v[184:187]
	v_mfma_f32_16x16x32_bf16 v[4:7], v[198:201], v[240:243], v[0:3]
	v_mfma_f32_16x16x32_bf16 v[0:3], v[202:205], v[236:239], v[124:127]
	v_mfma_f32_16x16x32_bf16 v[0:3], v[206:209], v[240:243], v[0:3]
	s_barrier
	s_add_u32 s59, s30, 0x200
	s_addc_u32 s60, s31, 0
	s_mov_b32 s61, 0
.LBB0_603:
	ds_read_b128 v[100:103], v217
	ds_read_b128 v[108:111], v217 offset:1024
	ds_read_b128 v[116:119], v217 offset:2048
	ds_read_b128 v[124:127], v217 offset:3072
	ds_read_b128 v[132:135], v218
	ds_read_b128 v[140:143], v218 offset:1024
	ds_read_b128 v[148:151], v218 offset:2048
	ds_read_b128 v[156:159], v218 offset:3072
	ds_read_b128 v[160:163], v219
	ds_read_b128 v[164:167], v219 offset:1024
	ds_read_b128 v[168:171], v219 offset:2048
	ds_read_b128 v[172:175], v219 offset:3072
	ds_read_b128 v[176:179], v219 offset:4096
	ds_read_b128 v[180:183], v219 offset:5120
	ds_read_b128 v[184:187], v219 offset:6144
	ds_read_b128 v[194:197], v219 offset:7168
	s_add_u32 s30, s36, 0x100
	s_addc_u32 s31, s37, 0
	s_cmp_eq_u32 s61, 28
	s_cselect_b32 s42, s9, s30
	s_cselect_b32 s43, s7, s31
	s_cselect_b32 s38, s25, s59
	s_cselect_b32 s39, s23, s60
	s_add_u32 s34, s42, 0x80
	s_addc_u32 s35, s43, 0
	s_add_u32 s40, s38, 0x80
	s_addc_u32 s41, s39, 0
	s_add_u32 s36, s36, 0x80080
	s_addc_u32 s37, s37, 0
	s_add_i32 m0, s48, 0xc000
	s_nop 0
	global_load_lds_dwordx4 v213, s[36:37]
	s_add_i32 m0, s48, 0xe000
	s_nop 0
	global_load_lds_dwordx4 v214, s[36:37]
	s_waitcnt vmcnt(8) lgkmcnt(0)
	s_barrier
	v_mfma_f32_16x16x32_bf16 v[152:155], v[100:103], v[160:163], v[152:155]
	v_mfma_f32_16x16x32_bf16 v[144:147], v[116:119], v[160:163], v[144:147]
	v_mfma_f32_16x16x32_bf16 v[112:115], v[116:119], v[168:171], v[112:115]
	v_mfma_f32_16x16x32_bf16 v[120:123], v[100:103], v[168:171], v[120:123]
	v_mfma_f32_16x16x32_bf16 v[92:95], v[100:103], v[176:179], v[92:95]
	v_mfma_f32_16x16x32_bf16 v[88:91], v[116:119], v[176:179], v[88:91]
	v_mfma_f32_16x16x32_bf16 v[72:75], v[116:119], v[184:187], v[72:75]
	v_mfma_f32_16x16x32_bf16 v[76:79], v[100:103], v[184:187], v[76:79]
	v_mfma_f32_16x16x32_bf16 v[152:155], v[108:111], v[164:167], v[152:155]
	v_mfma_f32_16x16x32_bf16 v[144:147], v[124:127], v[164:167], v[144:147]
	v_mfma_f32_16x16x32_bf16 v[112:115], v[124:127], v[172:175], v[112:115]
	v_mfma_f32_16x16x32_bf16 v[120:123], v[108:111], v[172:175], v[120:123]
	v_mfma_f32_16x16x32_bf16 v[92:95], v[108:111], v[180:183], v[92:95]
	v_mfma_f32_16x16x32_bf16 v[88:91], v[124:127], v[180:183], v[88:91]
	v_mfma_f32_16x16x32_bf16 v[72:75], v[124:127], v[194:197], v[72:75]
	v_mfma_f32_16x16x32_bf16 v[76:79], v[108:111], v[194:197], v[76:79]
	v_mfma_f32_16x16x32_bf16 v[136:139], v[132:135], v[160:163], v[136:139]
	v_mfma_f32_16x16x32_bf16 v[128:131], v[148:151], v[160:163], v[128:131]
	v_mfma_f32_16x16x32_bf16 v[96:99], v[148:151], v[168:171], v[96:99]
	v_mfma_f32_16x16x32_bf16 v[104:107], v[132:135], v[168:171], v[104:107]
	v_mfma_f32_16x16x32_bf16 v[84:87], v[132:135], v[176:179], v[84:87]
	v_mfma_f32_16x16x32_bf16 v[80:83], v[148:151], v[176:179], v[80:83]
	v_mfma_f32_16x16x32_bf16 v[64:67], v[148:151], v[184:187], v[64:67]
	v_mfma_f32_16x16x32_bf16 v[68:71], v[132:135], v[184:187], v[68:71]
	v_mfma_f32_16x16x32_bf16 v[136:139], v[140:143], v[164:167], v[136:139]
	v_mfma_f32_16x16x32_bf16 v[128:131], v[156:159], v[164:167], v[128:131]
	v_mfma_f32_16x16x32_bf16 v[96:99], v[156:159], v[172:175], v[96:99]
	v_mfma_f32_16x16x32_bf16 v[104:107], v[140:143], v[172:175], v[104:107]
	v_mfma_f32_16x16x32_bf16 v[84:87], v[140:143], v[180:183], v[84:87]
	v_mfma_f32_16x16x32_bf16 v[80:83], v[156:159], v[180:183], v[80:83]
	v_mfma_f32_16x16x32_bf16 v[64:67], v[156:159], v[194:197], v[64:67]
	v_mfma_f32_16x16x32_bf16 v[68:71], v[140:143], v[194:197], v[68:71]
	s_barrier
	ds_read_b128 v[160:163], v219 offset:16384
	ds_read_b128 v[164:167], v219 offset:17408
	ds_read_b128 v[168:171], v219 offset:18432
	ds_read_b128 v[172:175], v219 offset:19456
	ds_read_b128 v[176:179], v219 offset:20480
	ds_read_b128 v[180:183], v219 offset:21504
	ds_read_b128 v[184:187], v219 offset:22528
	ds_read_b128 v[194:197], v219 offset:23552
	s_add_i32 m0, s48, 0x10000
	s_nop 0
	global_load_lds_dwordx4 v213, s[38:39]
	s_add_i32 m0, s48, 0x12000
	s_nop 0
	global_load_lds_dwordx4 v214, s[38:39]
	s_add_u32 s36, s38, 0x80000
	s_addc_u32 s37, s39, 0
	s_add_i32 m0, s48, 0x14000
	s_nop 0
	global_load_lds_dwordx4 v213, s[36:37]
	s_add_i32 m0, s48, 0x16000
	s_nop 0
	global_load_lds_dwordx4 v214, s[36:37]
	s_add_i32 m0, s48, 0
	s_nop 0
	global_load_lds_dwordx4 v213, s[42:43]
	s_add_i32 m0, s48, 0x2000
	s_nop 0
	global_load_lds_dwordx4 v214, s[42:43]
	s_waitcnt vmcnt(8) lgkmcnt(0)
	s_barrier
	v_mfma_f32_16x16x32_bf16 v[60:63], v[100:103], v[160:163], v[60:63]
	v_mfma_f32_16x16x32_bf16 v[56:59], v[116:119], v[160:163], v[56:59]
	v_mfma_f32_16x16x32_bf16 v[40:43], v[116:119], v[168:171], v[40:43]
	v_mfma_f32_16x16x32_bf16 v[44:47], v[100:103], v[168:171], v[44:47]
	v_mfma_f32_16x16x32_bf16 v[28:31], v[100:103], v[176:179], v[28:31]
	v_mfma_f32_16x16x32_bf16 v[24:27], v[116:119], v[176:179], v[24:27]
	v_mfma_f32_16x16x32_bf16 v[8:11], v[116:119], v[184:187], v[8:11]
	v_mfma_f32_16x16x32_bf16 v[12:15], v[100:103], v[184:187], v[12:15]
	v_mfma_f32_16x16x32_bf16 v[60:63], v[108:111], v[164:167], v[60:63]
	v_mfma_f32_16x16x32_bf16 v[56:59], v[124:127], v[164:167], v[56:59]
	v_mfma_f32_16x16x32_bf16 v[40:43], v[124:127], v[172:175], v[40:43]
	v_mfma_f32_16x16x32_bf16 v[44:47], v[108:111], v[172:175], v[44:47]
	v_mfma_f32_16x16x32_bf16 v[28:31], v[108:111], v[180:183], v[28:31]
	v_mfma_f32_16x16x32_bf16 v[24:27], v[124:127], v[180:183], v[24:27]
	v_mfma_f32_16x16x32_bf16 v[8:11], v[124:127], v[194:197], v[8:11]
	v_mfma_f32_16x16x32_bf16 v[12:15], v[108:111], v[194:197], v[12:15]
	v_mfma_f32_16x16x32_bf16 v[52:55], v[132:135], v[160:163], v[52:55]
	v_mfma_f32_16x16x32_bf16 v[48:51], v[148:151], v[160:163], v[48:51]
	v_mfma_f32_16x16x32_bf16 v[32:35], v[148:151], v[168:171], v[32:35]
	v_mfma_f32_16x16x32_bf16 v[36:39], v[132:135], v[168:171], v[36:39]
	v_mfma_f32_16x16x32_bf16 v[20:23], v[132:135], v[176:179], v[20:23]
	v_mfma_f32_16x16x32_bf16 v[16:19], v[148:151], v[176:179], v[16:19]
	v_mfma_f32_16x16x32_bf16 v[0:3], v[148:151], v[184:187], v[0:3]
	v_mfma_f32_16x16x32_bf16 v[4:7], v[132:135], v[184:187], v[4:7]
	v_mfma_f32_16x16x32_bf16 v[52:55], v[140:143], v[164:167], v[52:55]
	v_mfma_f32_16x16x32_bf16 v[48:51], v[156:159], v[164:167], v[48:51]
	v_mfma_f32_16x16x32_bf16 v[32:35], v[156:159], v[172:175], v[32:35]
	v_mfma_f32_16x16x32_bf16 v[36:39], v[140:143], v[172:175], v[36:39]
	v_mfma_f32_16x16x32_bf16 v[20:23], v[140:143], v[180:183], v[20:23]
	v_mfma_f32_16x16x32_bf16 v[16:19], v[156:159], v[180:183], v[16:19]
	v_mfma_f32_16x16x32_bf16 v[0:3], v[156:159], v[194:197], v[0:3]
	v_mfma_f32_16x16x32_bf16 v[4:7], v[140:143], v[194:197], v[4:7]
	s_barrier
	ds_read_b128 v[100:103], v220
	ds_read_b128 v[108:111], v220 offset:1024
	ds_read_b128 v[116:119], v220 offset:2048
	ds_read_b128 v[124:127], v220 offset:3072
	ds_read_b128 v[132:135], v221
	ds_read_b128 v[140:143], v221 offset:1024
	ds_read_b128 v[148:151], v221 offset:2048
	ds_read_b128 v[156:159], v221 offset:3072
	ds_read_b128 v[160:163], v219 offset:32768
	ds_read_b128 v[164:167], v219 offset:33792
	ds_read_b128 v[168:171], v219 offset:34816
	ds_read_b128 v[172:175], v219 offset:35840
	ds_read_b128 v[176:179], v219 offset:36864
	ds_read_b128 v[180:183], v219 offset:37888
	ds_read_b128 v[184:187], v219 offset:38912
	ds_read_b128 v[194:197], v219 offset:39936
	s_add_u32 s36, s42, 0x80000
	s_addc_u32 s37, s43, 0
	s_add_i32 m0, s48, 0x4000
	s_nop 0
	global_load_lds_dwordx4 v213, s[36:37]
	s_add_i32 m0, s48, 0x6000
	s_nop 0
	global_load_lds_dwordx4 v214, s[36:37]
	s_waitcnt vmcnt(8) lgkmcnt(0)
	s_barrier
	v_mfma_f32_16x16x32_bf16 v[152:155], v[100:103], v[160:163], v[152:155]
	v_mfma_f32_16x16x32_bf16 v[144:147], v[116:119], v[160:163], v[144:147]
	v_mfma_f32_16x16x32_bf16 v[112:115], v[116:119], v[168:171], v[112:115]
	v_mfma_f32_16x16x32_bf16 v[120:123], v[100:103], v[168:171], v[120:123]
	v_mfma_f32_16x16x32_bf16 v[92:95], v[100:103], v[176:179], v[92:95]
	v_mfma_f32_16x16x32_bf16 v[88:91], v[116:119], v[176:179], v[88:91]
	v_mfma_f32_16x16x32_bf16 v[72:75], v[116:119], v[184:187], v[72:75]
	v_mfma_f32_16x16x32_bf16 v[76:79], v[100:103], v[184:187], v[76:79]
	v_mfma_f32_16x16x32_bf16 v[152:155], v[108:111], v[164:167], v[152:155]
	v_mfma_f32_16x16x32_bf16 v[144:147], v[124:127], v[164:167], v[144:147]
	v_mfma_f32_16x16x32_bf16 v[112:115], v[124:127], v[172:175], v[112:115]
	v_mfma_f32_16x16x32_bf16 v[120:123], v[108:111], v[172:175], v[120:123]
	v_mfma_f32_16x16x32_bf16 v[92:95], v[108:111], v[180:183], v[92:95]
	v_mfma_f32_16x16x32_bf16 v[88:91], v[124:127], v[180:183], v[88:91]
	v_mfma_f32_16x16x32_bf16 v[72:75], v[124:127], v[194:197], v[72:75]
	v_mfma_f32_16x16x32_bf16 v[76:79], v[108:111], v[194:197], v[76:79]
	v_mfma_f32_16x16x32_bf16 v[136:139], v[132:135], v[160:163], v[136:139]
	v_mfma_f32_16x16x32_bf16 v[128:131], v[148:151], v[160:163], v[128:131]
	v_mfma_f32_16x16x32_bf16 v[96:99], v[148:151], v[168:171], v[96:99]
	v_mfma_f32_16x16x32_bf16 v[104:107], v[132:135], v[168:171], v[104:107]
	v_mfma_f32_16x16x32_bf16 v[84:87], v[132:135], v[176:179], v[84:87]
	v_mfma_f32_16x16x32_bf16 v[80:83], v[148:151], v[176:179], v[80:83]
	v_mfma_f32_16x16x32_bf16 v[64:67], v[148:151], v[184:187], v[64:67]
	v_mfma_f32_16x16x32_bf16 v[68:71], v[132:135], v[184:187], v[68:71]
	v_mfma_f32_16x16x32_bf16 v[136:139], v[140:143], v[164:167], v[136:139]
	v_mfma_f32_16x16x32_bf16 v[128:131], v[156:159], v[164:167], v[128:131]
	v_mfma_f32_16x16x32_bf16 v[96:99], v[156:159], v[172:175], v[96:99]
	v_mfma_f32_16x16x32_bf16 v[104:107], v[140:143], v[172:175], v[104:107]
	v_mfma_f32_16x16x32_bf16 v[84:87], v[140:143], v[180:183], v[84:87]
	v_mfma_f32_16x16x32_bf16 v[80:83], v[156:159], v[180:183], v[80:83]
	v_mfma_f32_16x16x32_bf16 v[64:67], v[156:159], v[194:197], v[64:67]
	v_mfma_f32_16x16x32_bf16 v[68:71], v[140:143], v[194:197], v[68:71]
	s_barrier
	ds_read_b128 v[160:163], v219 offset:49152
	ds_read_b128 v[164:167], v219 offset:50176
	ds_read_b128 v[168:171], v219 offset:51200
	ds_read_b128 v[172:175], v219 offset:52224
	ds_read_b128 v[176:179], v219 offset:53248
	ds_read_b128 v[180:183], v219 offset:54272
	ds_read_b128 v[184:187], v219 offset:55296
	ds_read_b128 v[194:197], v219 offset:56320
	s_add_i32 m0, s48, 0x18000
	s_nop 0
	global_load_lds_dwordx4 v213, s[40:41]
	s_add_i32 m0, s48, 0x1a000
	s_nop 0
	global_load_lds_dwordx4 v214, s[40:41]
	s_add_u32 s36, s38, 0x80080
	s_addc_u32 s37, s39, 0
	s_add_i32 m0, s48, 0x1c000
	s_nop 0
	global_load_lds_dwordx4 v213, s[36:37]
	s_add_i32 m0, s48, 0x1e000
	s_nop 0
	global_load_lds_dwordx4 v214, s[36:37]
	s_add_i32 m0, s48, 0x8000
	s_nop 0
	global_load_lds_dwordx4 v213, s[34:35]
	s_add_i32 m0, s48, 0xa000
	s_nop 0
	global_load_lds_dwordx4 v214, s[34:35]
	s_add_i32 s61, s61, 2
	s_add_u32 s59, s59, 0x100
	s_addc_u32 s60, s60, 0
	s_cmp_gt_u32 s61, 29
	s_mov_b64 s[36:37], s[30:31]
	s_waitcnt vmcnt(8) lgkmcnt(0)
	s_barrier
	v_mfma_f32_16x16x32_bf16 v[60:63], v[100:103], v[160:163], v[60:63]
	v_mfma_f32_16x16x32_bf16 v[56:59], v[116:119], v[160:163], v[56:59]
	v_mfma_f32_16x16x32_bf16 v[40:43], v[116:119], v[168:171], v[40:43]
	v_mfma_f32_16x16x32_bf16 v[44:47], v[100:103], v[168:171], v[44:47]
	v_mfma_f32_16x16x32_bf16 v[28:31], v[100:103], v[176:179], v[28:31]
	v_mfma_f32_16x16x32_bf16 v[24:27], v[116:119], v[176:179], v[24:27]
	v_mfma_f32_16x16x32_bf16 v[8:11], v[116:119], v[184:187], v[8:11]
	v_mfma_f32_16x16x32_bf16 v[12:15], v[100:103], v[184:187], v[12:15]
	v_mfma_f32_16x16x32_bf16 v[60:63], v[108:111], v[164:167], v[60:63]
	v_mfma_f32_16x16x32_bf16 v[56:59], v[124:127], v[164:167], v[56:59]
	v_mfma_f32_16x16x32_bf16 v[40:43], v[124:127], v[172:175], v[40:43]
	v_mfma_f32_16x16x32_bf16 v[44:47], v[108:111], v[172:175], v[44:47]
	v_mfma_f32_16x16x32_bf16 v[28:31], v[108:111], v[180:183], v[28:31]
	v_mfma_f32_16x16x32_bf16 v[24:27], v[124:127], v[180:183], v[24:27]
	v_mfma_f32_16x16x32_bf16 v[8:11], v[124:127], v[194:197], v[8:11]
	v_mfma_f32_16x16x32_bf16 v[12:15], v[108:111], v[194:197], v[12:15]
	v_mfma_f32_16x16x32_bf16 v[52:55], v[132:135], v[160:163], v[52:55]
	v_mfma_f32_16x16x32_bf16 v[48:51], v[148:151], v[160:163], v[48:51]
	v_mfma_f32_16x16x32_bf16 v[32:35], v[148:151], v[168:171], v[32:35]
	v_mfma_f32_16x16x32_bf16 v[36:39], v[132:135], v[168:171], v[36:39]
	v_mfma_f32_16x16x32_bf16 v[20:23], v[132:135], v[176:179], v[20:23]
	v_mfma_f32_16x16x32_bf16 v[16:19], v[148:151], v[176:179], v[16:19]
	v_mfma_f32_16x16x32_bf16 v[0:3], v[148:151], v[184:187], v[0:3]
	v_mfma_f32_16x16x32_bf16 v[4:7], v[132:135], v[184:187], v[4:7]
	v_mfma_f32_16x16x32_bf16 v[52:55], v[140:143], v[164:167], v[52:55]
	v_mfma_f32_16x16x32_bf16 v[48:51], v[156:159], v[164:167], v[48:51]
	v_mfma_f32_16x16x32_bf16 v[32:35], v[156:159], v[172:175], v[32:35]
	v_mfma_f32_16x16x32_bf16 v[36:39], v[140:143], v[172:175], v[36:39]
	v_mfma_f32_16x16x32_bf16 v[20:23], v[140:143], v[180:183], v[20:23]
	v_mfma_f32_16x16x32_bf16 v[16:19], v[156:159], v[180:183], v[16:19]
	v_mfma_f32_16x16x32_bf16 v[0:3], v[156:159], v[194:197], v[0:3]
	v_mfma_f32_16x16x32_bf16 v[4:7], v[140:143], v[194:197], v[4:7]
	s_barrier
	s_cbranch_scc0 .LBB0_603
	s_and_b64 vcc, exec, s[20:21]
	s_cbranch_vccz .LBB0_606
	s_barrier

.LBB0_755:
	ds_read_b128 v[20:23], v205
	ds_read_b128 v[24:27], v205 offset:1024
	ds_read_b128 v[28:31], v205 offset:2048
	ds_read_b128 v[32:35], v205 offset:3072
	ds_read_b128 v[36:39], v204
	ds_read_b128 v[40:43], v204 offset:1024
	ds_read_b128 v[52:55], v204 offset:2048
	ds_read_b128 v[56:59], v204 offset:3072
	ds_read_b128 v[64:67], v206
	ds_read_b128 v[68:71], v206 offset:1024
	ds_read_b128 v[72:75], v206 offset:2048
	ds_read_b128 v[76:79], v206 offset:3072
	ds_read_b128 v[80:83], v206 offset:4096
	ds_read_b128 v[84:87], v206 offset:5120
	ds_read_b128 v[88:91], v206 offset:6144
	ds_read_b128 v[92:95], v206 offset:7168
	s_add_u32 s24, s26, 0x100
	s_addc_u32 s25, s27, 0
	s_and_b64 s[30:31], s[30:31], exec
	s_cselect_b32 s38, s59, s24
	s_cselect_b32 s39, s58, s25
	s_cselect_b32 s35, s15, s62
	s_cselect_b32 s34, s60, s61
	s_add_u32 s30, s38, 0x80
	s_addc_u32 s31, s39, 0
	s_add_u32 s36, s34, 0x80
	s_addc_u32 s37, s35, 0
	s_add_u32 s26, s26, 0x40080
	s_addc_u32 s27, s27, 0
	s_add_i32 m0, s46, 0xc000
	s_nop 0
	global_load_lds_dwordx4 v199, s[26:27]
	s_add_i32 m0, s46, 0xe000
	s_nop 0
	global_load_lds_dwordx4 v201, s[26:27]
	s_waitcnt vmcnt(8) lgkmcnt(0)
	s_barrier
	v_mfma_i32_16x16x64_i8 v[184:187], v[20:23], v[64:67], v[184:187]
	v_mfma_i32_16x16x64_i8 v[176:179], v[28:31], v[64:67], v[176:179]
	v_mfma_i32_16x16x64_i8 v[160:163], v[28:31], v[72:75], v[160:163]
	v_mfma_i32_16x16x64_i8 v[168:171], v[20:23], v[72:75], v[168:171]
	v_mfma_i32_16x16x64_i8 v[152:155], v[20:23], v[80:83], v[152:155]
	v_mfma_i32_16x16x64_i8 v[144:147], v[28:31], v[80:83], v[144:147]
	v_mfma_i32_16x16x64_i8 v[128:131], v[28:31], v[88:91], v[128:131]
	v_mfma_i32_16x16x64_i8 v[136:139], v[20:23], v[88:91], v[136:139]
	v_mfma_i32_16x16x64_i8 v[184:187], v[24:27], v[68:71], v[184:187]
	v_mfma_i32_16x16x64_i8 v[176:179], v[32:35], v[68:71], v[176:179]
	v_mfma_i32_16x16x64_i8 v[160:163], v[32:35], v[76:79], v[160:163]
	v_mfma_i32_16x16x64_i8 v[168:171], v[24:27], v[76:79], v[168:171]
	v_mfma_i32_16x16x64_i8 v[152:155], v[24:27], v[84:87], v[152:155]
	v_mfma_i32_16x16x64_i8 v[144:147], v[32:35], v[84:87], v[144:147]
	v_mfma_i32_16x16x64_i8 v[128:131], v[32:35], v[92:95], v[128:131]
	v_mfma_i32_16x16x64_i8 v[136:139], v[24:27], v[92:95], v[136:139]
	v_mfma_i32_16x16x64_i8 v[188:191], v[36:39], v[64:67], v[188:191]
	v_mfma_i32_16x16x64_i8 v[64:67], v[52:55], v[64:67], v[180:183]
	v_mfma_i32_16x16x64_i8 v[188:191], v[40:43], v[68:71], v[188:191]
	v_mfma_i32_16x16x64_i8 v[64:67], v[56:59], v[68:71], v[64:67]
	v_mfma_i32_16x16x64_i8 v[68:71], v[36:39], v[72:75], v[172:175]
	v_mfma_i32_16x16x64_i8 v[72:75], v[52:55], v[72:75], v[164:167]
	v_mfma_i32_16x16x64_i8 v[68:71], v[40:43], v[76:79], v[68:71]
	v_mfma_i32_16x16x64_i8 v[72:75], v[56:59], v[76:79], v[72:75]
	v_mfma_i32_16x16x64_i8 v[76:79], v[36:39], v[80:83], v[156:159]
	v_mfma_i32_16x16x64_i8 v[80:83], v[52:55], v[80:83], v[148:151]
	v_mfma_i32_16x16x64_i8 v[76:79], v[40:43], v[84:87], v[76:79]
	v_mfma_i32_16x16x64_i8 v[80:83], v[56:59], v[84:87], v[80:83]
	v_mfma_i32_16x16x64_i8 v[84:87], v[36:39], v[88:91], v[140:143]
	v_mfma_i32_16x16x64_i8 v[88:91], v[52:55], v[88:91], v[132:135]
	v_mfma_i32_16x16x64_i8 v[84:87], v[40:43], v[92:95], v[84:87]
	v_mfma_i32_16x16x64_i8 v[88:91], v[56:59], v[92:95], v[88:91]
	s_barrier
	ds_read_b128 v[92:95], v206 offset:16384
	ds_read_b128 v[132:135], v206 offset:17408
	ds_read_b128 v[140:143], v206 offset:18432
	ds_read_b128 v[148:151], v206 offset:19456
	ds_read_b128 v[156:159], v206 offset:20480
	ds_read_b128 v[164:167], v206 offset:21504
	ds_read_b128 v[172:175], v206 offset:22528
	ds_read_b128 v[180:183], v206 offset:23552
	s_add_i32 m0, s46, 0x10000
	s_nop 0
	global_load_lds_dwordx4 v200, s[34:35]
	s_add_i32 m0, s46, 0x12000
	s_nop 0
	global_load_lds_dwordx4 v202, s[34:35]
	s_add_u32 s26, s34, 0x40000
	s_addc_u32 s27, s35, 0
	s_add_i32 m0, s46, 0x14000
	s_nop 0
	global_load_lds_dwordx4 v200, s[26:27]
	s_add_i32 m0, s46, 0x16000
	s_nop 0
	global_load_lds_dwordx4 v202, s[26:27]
	s_add_i32 m0, s46, 0
	s_nop 0
	global_load_lds_dwordx4 v199, s[38:39]
	s_add_i32 m0, s46, 0x2000
	s_nop 0
	global_load_lds_dwordx4 v201, s[38:39]
	s_waitcnt vmcnt(8) lgkmcnt(0)
	s_barrier
	v_mfma_i32_16x16x64_i8 v[120:123], v[20:23], v[92:95], v[120:123]
	v_mfma_i32_16x16x64_i8 v[112:115], v[28:31], v[92:95], v[112:115]
	v_mfma_i32_16x16x64_i8 v[96:99], v[28:31], v[140:143], v[96:99]
	v_mfma_i32_16x16x64_i8 v[104:107], v[20:23], v[140:143], v[104:107]
	v_mfma_i32_16x16x64_i8 v[48:51], v[20:23], v[156:159], v[48:51]
	v_mfma_i32_16x16x64_i8 v[16:19], v[28:31], v[156:159], v[16:19]
	v_mfma_i32_16x16x64_i8 v[0:3], v[28:31], v[172:175], v[0:3]
	v_mfma_i32_16x16x64_i8 v[8:11], v[20:23], v[172:175], v[8:11]
	v_mfma_i32_16x16x64_i8 v[120:123], v[24:27], v[132:135], v[120:123]
	v_mfma_i32_16x16x64_i8 v[112:115], v[32:35], v[132:135], v[112:115]
	v_mfma_i32_16x16x64_i8 v[96:99], v[32:35], v[148:151], v[96:99]
	v_mfma_i32_16x16x64_i8 v[104:107], v[24:27], v[148:151], v[104:107]
	v_mfma_i32_16x16x64_i8 v[48:51], v[24:27], v[164:167], v[48:51]
	v_mfma_i32_16x16x64_i8 v[16:19], v[32:35], v[164:167], v[16:19]
	v_mfma_i32_16x16x64_i8 v[0:3], v[32:35], v[180:183], v[0:3]
	v_mfma_i32_16x16x64_i8 v[8:11], v[24:27], v[180:183], v[8:11]
	v_mfma_i32_16x16x64_i8 v[20:23], v[36:39], v[92:95], v[124:127]
	v_mfma_i32_16x16x64_i8 v[124:127], v[40:43], v[132:135], v[20:23]
	v_mfma_i32_16x16x64_i8 v[20:23], v[52:55], v[92:95], v[116:119]
	v_mfma_i32_16x16x64_i8 v[116:119], v[56:59], v[132:135], v[20:23]
	v_mfma_i32_16x16x64_i8 v[20:23], v[36:39], v[140:143], v[108:111]
	v_mfma_i32_16x16x64_i8 v[108:111], v[40:43], v[148:151], v[20:23]
	v_mfma_i32_16x16x64_i8 v[20:23], v[52:55], v[140:143], v[100:103]
	v_mfma_i32_16x16x64_i8 v[100:103], v[56:59], v[148:151], v[20:23]
	v_mfma_i32_16x16x64_i8 v[20:23], v[36:39], v[156:159], v[60:63]
	v_mfma_i32_16x16x64_i8 v[60:63], v[40:43], v[164:167], v[20:23]
	v_mfma_i32_16x16x64_i8 v[20:23], v[52:55], v[156:159], v[44:47]
	v_mfma_i32_16x16x64_i8 v[12:15], v[36:39], v[172:175], v[12:15]
	v_mfma_i32_16x16x64_i8 v[4:7], v[52:55], v[172:175], v[4:7]
	v_mfma_i32_16x16x64_i8 v[44:47], v[56:59], v[164:167], v[20:23]
	v_mfma_i32_16x16x64_i8 v[12:15], v[40:43], v[180:183], v[12:15]
	v_mfma_i32_16x16x64_i8 v[4:7], v[56:59], v[180:183], v[4:7]
	s_barrier
	ds_read_b128 v[36:39], v207
	ds_read_b128 v[28:31], v207 offset:1024
	ds_read_b128 v[24:27], v207 offset:2048
	ds_read_b128 v[20:23], v207 offset:3072
	ds_read_b128 v[56:59], v208
	ds_read_b128 v[52:55], v208 offset:1024
	ds_read_b128 v[40:43], v208 offset:2048
	ds_read_b128 v[32:35], v208 offset:3072
	ds_read_b128 v[92:95], v206 offset:32768
	ds_read_b128 v[132:135], v206 offset:33792
	ds_read_b128 v[140:143], v206 offset:34816
	ds_read_b128 v[148:151], v206 offset:35840
	ds_read_b128 v[192:195], v206 offset:36864
	ds_read_b128 v[210:213], v206 offset:37888
	ds_read_b128 v[214:217], v206 offset:38912
	ds_read_b128 v[218:221], v206 offset:39936
	s_add_u32 s26, s38, 0x40000
	s_addc_u32 s27, s39, 0
	s_add_i32 m0, s46, 0x4000
	s_nop 0
	global_load_lds_dwordx4 v199, s[26:27]
	s_add_i32 m0, s46, 0x6000
	s_nop 0
	global_load_lds_dwordx4 v201, s[26:27]
	s_waitcnt vmcnt(8) lgkmcnt(0)
	s_barrier
	v_mfma_i32_16x16x64_i8 v[156:159], v[36:39], v[92:95], v[184:187]
	v_mfma_i32_16x16x64_i8 v[184:187], v[28:31], v[132:135], v[156:159]
	v_mfma_i32_16x16x64_i8 v[156:159], v[24:27], v[92:95], v[176:179]
	v_mfma_i32_16x16x64_i8 v[176:179], v[20:23], v[132:135], v[156:159]
	v_mfma_i32_16x16x64_i8 v[156:159], v[36:39], v[140:143], v[168:171]
	v_mfma_i32_16x16x64_i8 v[168:171], v[28:31], v[148:151], v[156:159]
	v_mfma_i32_16x16x64_i8 v[156:159], v[24:27], v[140:143], v[160:163]
	v_mfma_i32_16x16x64_i8 v[152:155], v[36:39], v[192:195], v[152:155]
	v_mfma_i32_16x16x64_i8 v[144:147], v[24:27], v[192:195], v[144:147]
	v_mfma_i32_16x16x64_i8 v[136:139], v[36:39], v[214:217], v[136:139]
	v_mfma_i32_16x16x64_i8 v[128:131], v[24:27], v[214:217], v[128:131]
	v_mfma_i32_16x16x64_i8 v[160:163], v[20:23], v[148:151], v[156:159]
	v_mfma_i32_16x16x64_i8 v[152:155], v[28:31], v[210:213], v[152:155]
	v_mfma_i32_16x16x64_i8 v[144:147], v[20:23], v[210:213], v[144:147]
	v_mfma_i32_16x16x64_i8 v[136:139], v[28:31], v[218:221], v[136:139]
	v_mfma_i32_16x16x64_i8 v[128:131], v[20:23], v[218:221], v[128:131]
	v_mfma_i32_16x16x64_i8 v[64:67], v[40:43], v[92:95], v[64:67]
	v_mfma_i32_16x16x64_i8 v[180:183], v[32:35], v[132:135], v[64:67]
	v_mfma_i32_16x16x64_i8 v[64:67], v[56:59], v[140:143], v[68:71]
	v_mfma_i32_16x16x64_i8 v[172:175], v[52:55], v[148:151], v[64:67]
	v_mfma_i32_16x16x64_i8 v[64:67], v[40:43], v[140:143], v[72:75]
	v_mfma_i32_16x16x64_i8 v[156:159], v[56:59], v[92:95], v[188:191]
	v_mfma_i32_16x16x64_i8 v[164:167], v[32:35], v[148:151], v[64:67]
	v_mfma_i32_16x16x64_i8 v[64:67], v[56:59], v[192:195], v[76:79]
	v_mfma_i32_16x16x64_i8 v[188:191], v[52:55], v[132:135], v[156:159]
	v_mfma_i32_16x16x64_i8 v[156:159], v[52:55], v[210:213], v[64:67]
	v_mfma_i32_16x16x64_i8 v[64:67], v[40:43], v[192:195], v[80:83]
	v_mfma_i32_16x16x64_i8 v[148:151], v[32:35], v[210:213], v[64:67]
	v_mfma_i32_16x16x64_i8 v[64:67], v[56:59], v[214:217], v[84:87]
	v_mfma_i32_16x16x64_i8 v[140:143], v[52:55], v[218:221], v[64:67]
	v_mfma_i32_16x16x64_i8 v[64:67], v[40:43], v[214:217], v[88:91]
	v_mfma_i32_16x16x64_i8 v[132:135], v[32:35], v[218:221], v[64:67]
	s_barrier
	ds_read_b128 v[92:95], v206 offset:49152
	ds_read_b128 v[88:91], v206 offset:50176
	ds_read_b128 v[84:87], v206 offset:51200
	ds_read_b128 v[80:83], v206 offset:52224
	ds_read_b128 v[76:79], v206 offset:53248
	ds_read_b128 v[72:75], v206 offset:54272
	ds_read_b128 v[68:71], v206 offset:55296
	ds_read_b128 v[64:67], v206 offset:56320
	s_add_i32 m0, s46, 0x18000
	s_nop 0
	global_load_lds_dwordx4 v200, s[36:37]
	s_add_i32 m0, s46, 0x1a000
	s_nop 0
	global_load_lds_dwordx4 v202, s[36:37]
	s_add_u32 s26, s34, 0x40080
	s_addc_u32 s27, s35, 0
	s_add_i32 m0, s46, 0x1c000
	s_nop 0
	global_load_lds_dwordx4 v200, s[26:27]
	s_add_i32 m0, s46, 0x1e000
	s_nop 0
	global_load_lds_dwordx4 v202, s[26:27]
	s_add_i32 m0, s46, 0x8000
	s_nop 0
	global_load_lds_dwordx4 v199, s[30:31]
	s_add_i32 m0, s46, 0xa000
	s_nop 0
	global_load_lds_dwordx4 v201, s[30:31]
	s_add_i32 s17, s17, 2
	s_add_u32 s61, s61, 0x100
	s_addc_u32 s62, s62, 0
	s_cmp_gt_u32 s17, 13
	s_waitcnt vmcnt(8) lgkmcnt(0)
	s_barrier
	v_mfma_i32_16x16x64_i8 v[120:123], v[36:39], v[92:95], v[120:123]
	v_mfma_i32_16x16x64_i8 v[112:115], v[24:27], v[92:95], v[112:115]
	v_mfma_i32_16x16x64_i8 v[96:99], v[24:27], v[84:87], v[96:99]
	v_mfma_i32_16x16x64_i8 v[104:107], v[36:39], v[84:87], v[104:107]
	v_mfma_i32_16x16x64_i8 v[48:51], v[36:39], v[76:79], v[48:51]
	v_mfma_i32_16x16x64_i8 v[16:19], v[24:27], v[76:79], v[16:19]
	v_mfma_i32_16x16x64_i8 v[0:3], v[24:27], v[68:71], v[0:3]
	v_mfma_i32_16x16x64_i8 v[8:11], v[36:39], v[68:71], v[8:11]
	v_mfma_i32_16x16x64_i8 v[120:123], v[28:31], v[88:91], v[120:123]
	v_mfma_i32_16x16x64_i8 v[112:115], v[20:23], v[88:91], v[112:115]
	v_mfma_i32_16x16x64_i8 v[96:99], v[20:23], v[80:83], v[96:99]
	v_mfma_i32_16x16x64_i8 v[104:107], v[28:31], v[80:83], v[104:107]
	v_mfma_i32_16x16x64_i8 v[48:51], v[28:31], v[72:75], v[48:51]
	v_mfma_i32_16x16x64_i8 v[16:19], v[20:23], v[72:75], v[16:19]
	v_mfma_i32_16x16x64_i8 v[0:3], v[20:23], v[64:67], v[0:3]
	v_mfma_i32_16x16x64_i8 v[8:11], v[28:31], v[64:67], v[8:11]
	v_mfma_i32_16x16x64_i8 v[124:127], v[56:59], v[92:95], v[124:127]
	v_mfma_i32_16x16x64_i8 v[116:119], v[40:43], v[92:95], v[116:119]
	v_mfma_i32_16x16x64_i8 v[100:103], v[40:43], v[84:87], v[100:103]
	v_mfma_i32_16x16x64_i8 v[108:111], v[56:59], v[84:87], v[108:111]
	v_mfma_i32_16x16x64_i8 v[60:63], v[56:59], v[76:79], v[60:63]
	v_mfma_i32_16x16x64_i8 v[44:47], v[40:43], v[76:79], v[44:47]
	v_mfma_i32_16x16x64_i8 v[4:7], v[40:43], v[68:71], v[4:7]
	v_mfma_i32_16x16x64_i8 v[12:15], v[56:59], v[68:71], v[12:15]
	v_mfma_i32_16x16x64_i8 v[124:127], v[52:55], v[88:91], v[124:127]
	v_mfma_i32_16x16x64_i8 v[116:119], v[32:35], v[88:91], v[116:119]
	v_mfma_i32_16x16x64_i8 v[100:103], v[32:35], v[80:83], v[100:103]
	v_mfma_i32_16x16x64_i8 v[108:111], v[52:55], v[80:83], v[108:111]
	v_mfma_i32_16x16x64_i8 v[60:63], v[52:55], v[72:75], v[60:63]
	v_mfma_i32_16x16x64_i8 v[44:47], v[32:35], v[72:75], v[44:47]
	v_mfma_i32_16x16x64_i8 v[4:7], v[32:35], v[64:67], v[4:7]
	v_mfma_i32_16x16x64_i8 v[12:15], v[52:55], v[64:67], v[12:15]
	s_barrier
	s_cbranch_scc1 .LBB0_757
	s_mov_b64 s[26:27], s[24:25]
	s_branch .LBB0_753

.LBB0_837:
	s_waitcnt lgkmcnt(0)
	s_add_u32 s28, s22, 0x100
	s_addc_u32 s29, s23, 0
	s_add_u32 s52, s24, 0x100
	s_addc_u32 s53, s25, 0
	s_add_u32 s6, s22, 0x180
	s_addc_u32 s7, s23, 0
	s_add_u32 s26, s24, 0x180
	s_addc_u32 s27, s25, 0
	s_add_u32 s54, s22, 0x160080
	s_addc_u32 s55, s23, 0
	s_add_i32 m0, s36, 0xc000
	s_nop 0
	global_load_lds_dwordx4 v175, s[54:55]
	s_add_i32 m0, s36, 0xe000
	s_nop 0
	global_load_lds_dwordx4 v177, s[54:55]
	s_waitcnt vmcnt(8) lgkmcnt(0)
	s_barrier
	v_mfma_f32_16x16x32_bf16 v[88:91], v[0:3], v[56:59], 0
	v_mfma_f32_16x16x32_bf16 v[64:67], v[0:3], v[32:35], 0
	v_mfma_f32_16x16x32_bf16 v[68:71], v[8:11], v[32:35], 0
	v_mfma_f32_16x16x32_bf16 v[72:75], v[0:3], v[40:43], 0
	v_mfma_f32_16x16x32_bf16 v[76:79], v[8:11], v[40:43], 0
	v_mfma_f32_16x16x32_bf16 v[80:83], v[0:3], v[48:51], 0
	v_mfma_f32_16x16x32_bf16 v[84:87], v[8:11], v[48:51], 0
	v_mfma_f32_16x16x32_bf16 v[96:99], v[4:7], v[60:63], v[88:91]
	v_mfma_f32_16x16x32_bf16 v[88:91], v[8:11], v[56:59], 0
	v_mfma_f32_16x16x32_bf16 v[64:67], v[4:7], v[36:39], v[64:67]
	v_mfma_f32_16x16x32_bf16 v[68:71], v[12:15], v[36:39], v[68:71]
	v_mfma_f32_16x16x32_bf16 v[72:75], v[4:7], v[44:47], v[72:75]
	v_mfma_f32_16x16x32_bf16 v[76:79], v[12:15], v[44:47], v[76:79]
	v_mfma_f32_16x16x32_bf16 v[80:83], v[4:7], v[52:55], v[80:83]
	v_mfma_f32_16x16x32_bf16 v[84:87], v[12:15], v[52:55], v[84:87]
	v_mfma_f32_16x16x32_bf16 v[100:103], v[12:15], v[60:63], v[88:91]
	v_mfma_f32_16x16x32_bf16 v[88:91], v[16:19], v[32:35], 0
	v_mfma_f32_16x16x32_bf16 v[32:35], v[24:27], v[32:35], 0
	v_mfma_f32_16x16x32_bf16 v[112:115], v[20:23], v[36:39], v[88:91]
	v_mfma_f32_16x16x32_bf16 v[32:35], v[28:31], v[36:39], v[32:35]
	v_mfma_f32_16x16x32_bf16 v[36:39], v[16:19], v[40:43], 0
	v_mfma_f32_16x16x32_bf16 v[40:43], v[24:27], v[40:43], 0
	v_mfma_f32_16x16x32_bf16 v[36:39], v[20:23], v[44:47], v[36:39]
	v_mfma_f32_16x16x32_bf16 v[40:43], v[28:31], v[44:47], v[40:43]
	v_mfma_f32_16x16x32_bf16 v[44:47], v[16:19], v[48:51], 0
	v_mfma_f32_16x16x32_bf16 v[48:51], v[24:27], v[48:51], 0
	v_mfma_f32_16x16x32_bf16 v[44:47], v[20:23], v[52:55], v[44:47]
	v_mfma_f32_16x16x32_bf16 v[48:51], v[28:31], v[52:55], v[48:51]
	v_mfma_f32_16x16x32_bf16 v[52:55], v[16:19], v[56:59], 0
	v_mfma_f32_16x16x32_bf16 v[56:59], v[24:27], v[56:59], 0
	v_mfma_f32_16x16x32_bf16 v[52:55], v[20:23], v[60:63], v[52:55]
	v_mfma_f32_16x16x32_bf16 v[56:59], v[28:31], v[60:63], v[56:59]
	s_barrier
	ds_read_b128 v[60:63], v183 offset:16384
	ds_read_b128 v[88:91], v183 offset:17408
	ds_read_b128 v[92:95], v183 offset:18432
	ds_read_b128 v[104:107], v183 offset:19456
	ds_read_b128 v[108:111], v183 offset:20480
	ds_read_b128 v[116:119], v183 offset:21504
	ds_read_b128 v[120:123], v183 offset:22528
	ds_read_b128 v[124:127], v183 offset:23552
	s_add_i32 m0, s36, 0x10000
	s_nop 0
	global_load_lds_dwordx4 v176, s[52:53]
	s_add_i32 m0, s36, 0x12000
	s_nop 0
	global_load_lds_dwordx4 v178, s[52:53]
	s_add_u32 s52, s24, 0x160100
	s_addc_u32 s53, s25, 0
	s_add_i32 m0, s36, 0x14000
	s_nop 0
	global_load_lds_dwordx4 v176, s[52:53]
	s_add_i32 m0, s36, 0x16000
	s_nop 0
	global_load_lds_dwordx4 v178, s[52:53]
	s_add_i32 m0, s36, 0
	s_nop 0
	global_load_lds_dwordx4 v175, s[28:29]
	s_add_i32 m0, s36, 0x2000
	s_nop 0
	global_load_lds_dwordx4 v177, s[28:29]
	s_waitcnt vmcnt(8) lgkmcnt(0)
	s_barrier
	v_mfma_f32_16x16x32_bf16 v[128:131], v[0:3], v[60:63], 0
	v_mfma_f32_16x16x32_bf16 v[136:139], v[4:7], v[88:91], v[128:131]
	v_mfma_f32_16x16x32_bf16 v[128:131], v[8:11], v[60:63], 0
	v_mfma_f32_16x16x32_bf16 v[140:143], v[12:15], v[88:91], v[128:131]
	v_mfma_f32_16x16x32_bf16 v[128:131], v[0:3], v[92:95], 0
	v_mfma_f32_16x16x32_bf16 v[144:147], v[4:7], v[104:107], v[128:131]
	v_mfma_f32_16x16x32_bf16 v[128:131], v[8:11], v[92:95], 0
	v_mfma_f32_16x16x32_bf16 v[148:151], v[12:15], v[104:107], v[128:131]
	v_mfma_f32_16x16x32_bf16 v[128:131], v[0:3], v[108:111], 0
	v_mfma_f32_16x16x32_bf16 v[0:3], v[0:3], v[120:123], 0
	v_mfma_f32_16x16x32_bf16 v[156:159], v[4:7], v[116:119], v[128:131]
	v_mfma_f32_16x16x32_bf16 v[0:3], v[4:7], v[124:127], v[0:3]
	v_mfma_f32_16x16x32_bf16 v[4:7], v[8:11], v[120:123], 0
	v_mfma_f32_16x16x32_bf16 v[128:131], v[8:11], v[108:111], 0
	v_mfma_f32_16x16x32_bf16 v[4:7], v[12:15], v[124:127], v[4:7]
	v_mfma_f32_16x16x32_bf16 v[160:163], v[12:15], v[116:119], v[128:131]
	v_mfma_f32_16x16x32_bf16 v[8:11], v[16:19], v[60:63], 0
	v_mfma_f32_16x16x32_bf16 v[164:167], v[20:23], v[88:91], v[8:11]
	v_mfma_f32_16x16x32_bf16 v[8:11], v[24:27], v[60:63], 0
	v_mfma_f32_16x16x32_bf16 v[168:171], v[28:31], v[88:91], v[8:11]
	v_mfma_f32_16x16x32_bf16 v[8:11], v[16:19], v[92:95], 0
	v_mfma_f32_16x16x32_bf16 v[188:191], v[20:23], v[104:107], v[8:11]
	v_mfma_f32_16x16x32_bf16 v[8:11], v[24:27], v[92:95], 0
	v_mfma_f32_16x16x32_bf16 v[192:195], v[28:31], v[104:107], v[8:11]
	v_mfma_f32_16x16x32_bf16 v[8:11], v[16:19], v[108:111], 0
	v_mfma_f32_16x16x32_bf16 v[196:199], v[20:23], v[116:119], v[8:11]
	v_mfma_f32_16x16x32_bf16 v[8:11], v[24:27], v[108:111], 0
	v_mfma_f32_16x16x32_bf16 v[116:119], v[28:31], v[116:119], v[8:11]
	v_mfma_f32_16x16x32_bf16 v[8:11], v[16:19], v[120:123], 0
	v_mfma_f32_16x16x32_bf16 v[200:203], v[20:23], v[124:127], v[8:11]
	v_mfma_f32_16x16x32_bf16 v[8:11], v[24:27], v[120:123], 0
	v_mfma_f32_16x16x32_bf16 v[204:207], v[28:31], v[124:127], v[8:11]
	s_barrier
	s_nop 4
	ds_read_b128 v[8:11], v184
	ds_read_b128 v[12:15], v184 offset:1024
	ds_read_b128 v[16:19], v184 offset:2048
	ds_read_b128 v[20:23], v184 offset:3072
	ds_read_b128 v[208:211], v185
	ds_read_b128 v[212:215], v185 offset:1024
	ds_read_b128 v[216:219], v185 offset:2048
	ds_read_b128 v[220:223], v185 offset:3072
	ds_read_b128 v[24:27], v183 offset:32768
	ds_read_b128 v[28:31], v183 offset:33792
	ds_read_b128 v[60:63], v183 offset:34816
	ds_read_b128 v[224:227], v183 offset:35840
	ds_read_b128 v[228:231], v183 offset:36864
	ds_read_b128 v[232:235], v183 offset:37888
	ds_read_b128 v[236:239], v183 offset:38912
	ds_read_b128 v[240:243], v183 offset:39936
	s_add_u32 s28, s22, 0x160100
	s_addc_u32 s29, s23, 0
	s_add_i32 m0, s36, 0x4000
	s_nop 0
	global_load_lds_dwordx4 v175, s[28:29]
	s_add_i32 m0, s36, 0x6000
	s_nop 0
	global_load_lds_dwordx4 v177, s[28:29]
	s_waitcnt vmcnt(8) lgkmcnt(0)
	s_barrier
	v_mfma_f32_16x16x32_bf16 v[64:67], v[8:11], v[24:27], v[64:67]
	v_mfma_f32_16x16x32_bf16 v[132:135], v[12:15], v[28:31], v[64:67]
	v_mfma_f32_16x16x32_bf16 v[64:67], v[16:19], v[24:27], v[68:71]
	v_mfma_f32_16x16x32_bf16 v[128:131], v[20:23], v[28:31], v[64:67]
	v_mfma_f32_16x16x32_bf16 v[64:67], v[8:11], v[60:63], v[72:75]
	v_mfma_f32_16x16x32_bf16 v[108:111], v[12:15], v[224:227], v[64:67]
	v_mfma_f32_16x16x32_bf16 v[64:67], v[16:19], v[60:63], v[76:79]
	v_mfma_f32_16x16x32_bf16 v[104:107], v[20:23], v[224:227], v[64:67]
	v_mfma_f32_16x16x32_bf16 v[64:67], v[8:11], v[228:231], v[80:83]
	v_mfma_f32_16x16x32_bf16 v[92:95], v[12:15], v[232:235], v[64:67]
	v_mfma_f32_16x16x32_bf16 v[64:67], v[16:19], v[228:231], v[84:87]
	v_mfma_f32_16x16x32_bf16 v[88:91], v[20:23], v[232:235], v[64:67]
	v_mfma_f32_16x16x32_bf16 v[64:67], v[8:11], v[236:239], v[96:99]
	v_mfma_f32_16x16x32_bf16 v[76:79], v[12:15], v[240:243], v[64:67]
	v_mfma_f32_16x16x32_bf16 v[64:67], v[16:19], v[236:239], v[100:103]
	v_mfma_f32_16x16x32_bf16 v[72:75], v[20:23], v[240:243], v[64:67]
	v_mfma_f32_16x16x32_bf16 v[64:67], v[208:211], v[24:27], v[112:115]
	v_mfma_f32_16x16x32_bf16 v[24:27], v[216:219], v[24:27], v[32:35]
	v_mfma_f32_16x16x32_bf16 v[120:123], v[220:223], v[28:31], v[24:27]
	v_mfma_f32_16x16x32_bf16 v[24:27], v[208:211], v[60:63], v[36:39]
	v_mfma_f32_16x16x32_bf16 v[100:103], v[212:215], v[224:227], v[24:27]
	v_mfma_f32_16x16x32_bf16 v[24:27], v[216:219], v[60:63], v[40:43]
	v_mfma_f32_16x16x32_bf16 v[96:99], v[220:223], v[224:227], v[24:27]
	v_mfma_f32_16x16x32_bf16 v[24:27], v[208:211], v[228:231], v[44:47]
	v_mfma_f32_16x16x32_bf16 v[84:87], v[212:215], v[232:235], v[24:27]
	v_mfma_f32_16x16x32_bf16 v[24:27], v[216:219], v[228:231], v[48:51]
	v_mfma_f32_16x16x32_bf16 v[80:83], v[220:223], v[232:235], v[24:27]
	v_mfma_f32_16x16x32_bf16 v[24:27], v[208:211], v[236:239], v[52:55]
	v_mfma_f32_16x16x32_bf16 v[68:71], v[212:215], v[240:243], v[24:27]
	v_mfma_f32_16x16x32_bf16 v[24:27], v[216:219], v[236:239], v[56:59]
	v_mfma_f32_16x16x32_bf16 v[124:127], v[212:215], v[28:31], v[64:67]
	v_mfma_f32_16x16x32_bf16 v[64:67], v[220:223], v[240:243], v[24:27]
	s_barrier
	ds_read_b128 v[32:35], v183 offset:49152
	ds_read_b128 v[36:39], v183 offset:50176
	ds_read_b128 v[112:115], v183 offset:51200
	ds_read_b128 v[224:227], v183 offset:52224
	ds_read_b128 v[228:231], v183 offset:53248
	ds_read_b128 v[232:235], v183 offset:54272
	ds_read_b128 v[236:239], v183 offset:55296
	ds_read_b128 v[240:243], v183 offset:56320
	s_add_i32 m0, s36, 0x18000
	s_nop 0
	global_load_lds_dwordx4 v176, s[26:27]
	s_add_i32 m0, s36, 0x1a000
	s_nop 0
	global_load_lds_dwordx4 v178, s[26:27]
	s_add_u32 s26, s24, 0x160180
	s_addc_u32 s27, s25, 0
	s_add_i32 m0, s36, 0x1c000
	s_nop 0
	global_load_lds_dwordx4 v176, s[26:27]
	s_add_i32 m0, s36, 0x1e000
	s_nop 0
	global_load_lds_dwordx4 v178, s[26:27]
	s_add_i32 m0, s36, 0x8000
	s_nop 0
	global_load_lds_dwordx4 v175, s[6:7]
	s_add_i32 m0, s36, 0xa000
	s_nop 0
	global_load_lds_dwordx4 v177, s[6:7]
	s_waitcnt vmcnt(8) lgkmcnt(0)
	s_barrier
	v_mfma_f32_16x16x32_bf16 v[24:27], v[8:11], v[32:35], v[136:139]
	v_mfma_f32_16x16x32_bf16 v[60:63], v[12:15], v[36:39], v[24:27]
	v_mfma_f32_16x16x32_bf16 v[24:27], v[16:19], v[32:35], v[140:143]
	v_mfma_f32_16x16x32_bf16 v[56:59], v[20:23], v[36:39], v[24:27]
	v_mfma_f32_16x16x32_bf16 v[24:27], v[8:11], v[112:115], v[144:147]
	v_mfma_f32_16x16x32_bf16 v[44:47], v[12:15], v[224:227], v[24:27]
	v_mfma_f32_16x16x32_bf16 v[24:27], v[16:19], v[112:115], v[148:151]
	v_mfma_f32_16x16x32_bf16 v[40:43], v[20:23], v[224:227], v[24:27]
	v_mfma_f32_16x16x32_bf16 v[24:27], v[8:11], v[228:231], v[156:159]
	v_mfma_f32_16x16x32_bf16 v[0:3], v[8:11], v[236:239], v[0:3]
	v_mfma_f32_16x16x32_bf16 v[28:31], v[12:15], v[232:235], v[24:27]
	v_mfma_f32_16x16x32_bf16 v[24:27], v[16:19], v[228:231], v[160:163]
	v_mfma_f32_16x16x32_bf16 v[12:15], v[12:15], v[240:243], v[0:3]
	v_mfma_f32_16x16x32_bf16 v[0:3], v[16:19], v[236:239], v[4:7]
	v_mfma_f32_16x16x32_bf16 v[24:27], v[20:23], v[232:235], v[24:27]
	v_mfma_f32_16x16x32_bf16 v[8:11], v[20:23], v[240:243], v[0:3]
	v_mfma_f32_16x16x32_bf16 v[0:3], v[208:211], v[32:35], v[164:167]
	v_mfma_f32_16x16x32_bf16 v[52:55], v[212:215], v[36:39], v[0:3]
	v_mfma_f32_16x16x32_bf16 v[0:3], v[216:219], v[32:35], v[168:171]
	v_mfma_f32_16x16x32_bf16 v[48:51], v[220:223], v[36:39], v[0:3]
	v_mfma_f32_16x16x32_bf16 v[0:3], v[208:211], v[112:115], v[188:191]
	v_mfma_f32_16x16x32_bf16 v[36:39], v[212:215], v[224:227], v[0:3]
	v_mfma_f32_16x16x32_bf16 v[0:3], v[216:219], v[112:115], v[192:195]
	v_mfma_f32_16x16x32_bf16 v[32:35], v[220:223], v[224:227], v[0:3]
	v_mfma_f32_16x16x32_bf16 v[0:3], v[208:211], v[228:231], v[196:199]
	v_mfma_f32_16x16x32_bf16 v[20:23], v[212:215], v[232:235], v[0:3]
	v_mfma_f32_16x16x32_bf16 v[0:3], v[216:219], v[228:231], v[116:119]
	v_mfma_f32_16x16x32_bf16 v[16:19], v[220:223], v[232:235], v[0:3]
	v_mfma_f32_16x16x32_bf16 v[0:3], v[208:211], v[236:239], v[200:203]
	v_mfma_f32_16x16x32_bf16 v[4:7], v[212:215], v[240:243], v[0:3]
	v_mfma_f32_16x16x32_bf16 v[0:3], v[216:219], v[236:239], v[204:207]
	v_mfma_f32_16x16x32_bf16 v[0:3], v[220:223], v[240:243], v[0:3]
	s_barrier
	s_add_u32 s51, s22, 0x200
	s_addc_u32 s52, s23, 0
	s_add_u32 s53, s24, 0x200
	s_addc_u32 s54, s25, 0
	s_add_u32 s6, s22, 0x160180
	s_addc_u32 s7, s23, 0
	s_mov_b32 s55, 0

.LBB0_933:
	ds_read_b128 v[0:3], v227
	ds_read_b128 v[4:7], v227 offset:1024
	ds_read_b128 v[8:11], v227 offset:2048
	ds_read_b128 v[12:15], v227 offset:3072
	ds_read_b128 v[16:19], v226
	ds_read_b128 v[20:23], v226 offset:1024
	ds_read_b128 v[24:27], v226 offset:2048
	ds_read_b128 v[28:31], v226 offset:3072
	ds_read_b128 v[32:35], v228
	ds_read_b128 v[36:39], v228 offset:1024
	ds_read_b128 v[40:43], v228 offset:2048
	ds_read_b128 v[44:47], v228 offset:3072
	ds_read_b128 v[48:51], v228 offset:4096
	ds_read_b128 v[52:55], v228 offset:5120
	ds_read_b128 v[56:59], v228 offset:6144
	ds_read_b128 v[60:63], v228 offset:7168
	s_add_u32 s42, s46, 0x100
	s_addc_u32 s43, s47, 0
	s_and_b64 s[48:49], s[48:49], exec
	s_cselect_b32 s54, s76, s42
	s_cselect_b32 s55, s9, s43
	s_cselect_b32 s51, s35, s80
	s_cselect_b32 s50, s77, s79
	s_add_u32 s48, s54, 0x80
	s_addc_u32 s49, s55, 0
	s_add_u32 s52, s50, 0x80
	s_addc_u32 s53, s51, 0
	s_add_u32 s46, s46, 0x40080
	s_addc_u32 s47, s47, 0
	s_add_i32 m0, s31, 0xc000
	s_nop 0
	global_load_lds_dwordx4 v219, s[46:47]
	s_add_i32 m0, s31, 0xe000
	s_nop 0
	global_load_lds_dwordx4 v221, s[46:47]
	s_waitcnt vmcnt(8) lgkmcnt(0)
	s_barrier
	v_mfma_i32_16x16x64_i8 v[180:183], v[8:11], v[40:43], v[180:183]
	v_mfma_i32_16x16x64_i8 v[164:167], v[0:3], v[48:51], v[164:167]
	v_mfma_i32_16x16x64_i8 v[148:151], v[0:3], v[56:59], v[148:151]
	v_mfma_i32_16x16x64_i8 v[160:163], v[8:11], v[48:51], v[160:163]
	v_mfma_i32_16x16x64_i8 v[144:147], v[8:11], v[56:59], v[144:147]
	v_mfma_i32_16x16x64_i8 v[88:91], v[0:3], v[32:35], v[200:203]
	v_mfma_i32_16x16x64_i8 v[168:171], v[0:3], v[40:43], v[184:187]
	v_mfma_i32_16x16x64_i8 v[124:127], v[8:11], v[32:35], v[196:199]
	v_mfma_i32_16x16x64_i8 v[180:183], v[12:15], v[44:47], v[180:183]
	v_mfma_i32_16x16x64_i8 v[164:167], v[4:7], v[52:55], v[164:167]
	v_mfma_i32_16x16x64_i8 v[148:151], v[4:7], v[60:63], v[148:151]
	v_mfma_i32_16x16x64_i8 v[160:163], v[12:15], v[52:55], v[160:163]
	v_mfma_i32_16x16x64_i8 v[144:147], v[12:15], v[60:63], v[144:147]
	v_mfma_i32_16x16x64_i8 v[88:91], v[4:7], v[36:39], v[88:91]
	v_mfma_i32_16x16x64_i8 v[168:171], v[4:7], v[44:47], v[168:171]
	v_mfma_i32_16x16x64_i8 v[124:127], v[12:15], v[36:39], v[124:127]
	v_mfma_i32_16x16x64_i8 v[184:187], v[16:19], v[32:35], v[192:195]
	v_mfma_i32_16x16x64_i8 v[32:35], v[24:27], v[32:35], v[188:191]
	v_mfma_i32_16x16x64_i8 v[192:195], v[20:23], v[36:39], v[184:187]
	v_mfma_i32_16x16x64_i8 v[32:35], v[28:31], v[36:39], v[32:35]
	v_mfma_i32_16x16x64_i8 v[36:39], v[16:19], v[40:43], v[176:179]
	v_mfma_i32_16x16x64_i8 v[40:43], v[24:27], v[40:43], v[172:175]
	v_mfma_i32_16x16x64_i8 v[36:39], v[20:23], v[44:47], v[36:39]
	v_mfma_i32_16x16x64_i8 v[40:43], v[28:31], v[44:47], v[40:43]
	v_mfma_i32_16x16x64_i8 v[44:47], v[16:19], v[48:51], v[156:159]
	v_mfma_i32_16x16x64_i8 v[48:51], v[24:27], v[48:51], v[152:155]
	v_mfma_i32_16x16x64_i8 v[44:47], v[20:23], v[52:55], v[44:47]
	v_mfma_i32_16x16x64_i8 v[48:51], v[28:31], v[52:55], v[48:51]
	v_mfma_i32_16x16x64_i8 v[52:55], v[16:19], v[56:59], v[140:143]
	v_mfma_i32_16x16x64_i8 v[56:59], v[24:27], v[56:59], v[136:139]
	v_mfma_i32_16x16x64_i8 v[52:55], v[20:23], v[60:63], v[52:55]
	v_mfma_i32_16x16x64_i8 v[56:59], v[28:31], v[60:63], v[56:59]
	s_barrier
	ds_read_b128 v[60:63], v228 offset:16384
	ds_read_b128 v[136:139], v228 offset:17408
	ds_read_b128 v[140:143], v228 offset:18432
	ds_read_b128 v[152:155], v228 offset:19456
	ds_read_b128 v[156:159], v228 offset:20480
	ds_read_b128 v[172:175], v228 offset:21504
	ds_read_b128 v[176:179], v228 offset:22528
	ds_read_b128 v[184:187], v228 offset:23552
	s_add_i32 m0, s31, 0x10000
	s_nop 0
	global_load_lds_dwordx4 v220, s[50:51]
	s_add_i32 m0, s31, 0x12000
	s_nop 0
	global_load_lds_dwordx4 v222, s[50:51]
	s_add_u32 s46, s50, 0x40000
	s_addc_u32 s47, s51, 0
	s_add_i32 m0, s31, 0x14000
	s_nop 0
	global_load_lds_dwordx4 v220, s[46:47]
	s_add_i32 m0, s31, 0x16000
	s_nop 0
	global_load_lds_dwordx4 v222, s[46:47]
	s_add_i32 m0, s31, 0
	s_nop 0
	global_load_lds_dwordx4 v219, s[54:55]
	s_add_i32 m0, s31, 0x2000
	s_nop 0
	global_load_lds_dwordx4 v221, s[54:55]
	s_waitcnt vmcnt(8) lgkmcnt(0)
	s_barrier
	v_mfma_i32_16x16x64_i8 v[132:135], v[0:3], v[60:63], v[132:135]
	v_mfma_i32_16x16x64_i8 v[112:115], v[0:3], v[140:143], v[112:115]
	v_mfma_i32_16x16x64_i8 v[96:99], v[0:3], v[156:159], v[96:99]
	v_mfma_i32_16x16x64_i8 v[0:3], v[0:3], v[176:179], v[76:79]
	v_mfma_i32_16x16x64_i8 v[128:131], v[8:11], v[60:63], v[128:131]
	v_mfma_i32_16x16x64_i8 v[108:111], v[8:11], v[140:143], v[108:111]
	v_mfma_i32_16x16x64_i8 v[92:95], v[8:11], v[156:159], v[92:95]
	v_mfma_i32_16x16x64_i8 v[76:79], v[4:7], v[184:187], v[0:3]
	v_mfma_i32_16x16x64_i8 v[0:3], v[8:11], v[176:179], v[72:75]
	v_mfma_i32_16x16x64_i8 v[132:135], v[4:7], v[136:139], v[132:135]
	v_mfma_i32_16x16x64_i8 v[128:131], v[12:15], v[136:139], v[128:131]
	v_mfma_i32_16x16x64_i8 v[112:115], v[4:7], v[152:155], v[112:115]
	v_mfma_i32_16x16x64_i8 v[108:111], v[12:15], v[152:155], v[108:111]
	v_mfma_i32_16x16x64_i8 v[96:99], v[4:7], v[172:175], v[96:99]
	v_mfma_i32_16x16x64_i8 v[92:95], v[12:15], v[172:175], v[92:95]
	v_mfma_i32_16x16x64_i8 v[72:75], v[12:15], v[184:187], v[0:3]
	v_mfma_i32_16x16x64_i8 v[0:3], v[16:19], v[60:63], v[120:123]
	v_mfma_i32_16x16x64_i8 v[120:123], v[20:23], v[136:139], v[0:3]
	v_mfma_i32_16x16x64_i8 v[0:3], v[24:27], v[60:63], v[116:119]
	v_mfma_i32_16x16x64_i8 v[116:119], v[28:31], v[136:139], v[0:3]
	v_mfma_i32_16x16x64_i8 v[0:3], v[16:19], v[140:143], v[104:107]
	v_mfma_i32_16x16x64_i8 v[104:107], v[20:23], v[152:155], v[0:3]
	v_mfma_i32_16x16x64_i8 v[0:3], v[24:27], v[140:143], v[100:103]
	v_mfma_i32_16x16x64_i8 v[100:103], v[28:31], v[152:155], v[0:3]
	v_mfma_i32_16x16x64_i8 v[0:3], v[16:19], v[156:159], v[84:87]
	v_mfma_i32_16x16x64_i8 v[84:87], v[20:23], v[172:175], v[0:3]
	v_mfma_i32_16x16x64_i8 v[0:3], v[24:27], v[156:159], v[80:83]
	v_mfma_i32_16x16x64_i8 v[80:83], v[28:31], v[172:175], v[0:3]
	v_mfma_i32_16x16x64_i8 v[0:3], v[16:19], v[176:179], v[68:71]
	v_mfma_i32_16x16x64_i8 v[68:71], v[20:23], v[184:187], v[0:3]
	v_mfma_i32_16x16x64_i8 v[0:3], v[24:27], v[176:179], v[64:67]
	v_mfma_i32_16x16x64_i8 v[64:67], v[28:31], v[184:187], v[0:3]
	s_barrier
	ds_read_b128 v[16:19], v229
	ds_read_b128 v[8:11], v229 offset:1024
	ds_read_b128 v[4:7], v229 offset:2048
	s_nop 1
	ds_read_b128 v[0:3], v229 offset:3072
	ds_read_b128 v[28:31], v230
	ds_read_b128 v[24:27], v230 offset:1024
	ds_read_b128 v[20:23], v230 offset:2048
	ds_read_b128 v[12:15], v230 offset:3072
	ds_read_b128 v[60:63], v228 offset:32768
	ds_read_b128 v[136:139], v228 offset:33792
	ds_read_b128 v[140:143], v228 offset:34816
	ds_read_b128 v[152:155], v228 offset:35840
	ds_read_b128 v[204:207], v228 offset:36864
	ds_read_b128 v[208:211], v228 offset:37888
	ds_read_b128 v[214:217], v228 offset:38912
	ds_read_b128 v[232:235], v228 offset:39936
	s_add_u32 s46, s54, 0x40000
	s_addc_u32 s47, s55, 0
	s_add_i32 m0, s31, 0x4000
	s_nop 0
	global_load_lds_dwordx4 v219, s[46:47]
	s_add_i32 m0, s31, 0x6000
	s_nop 0
	global_load_lds_dwordx4 v221, s[46:47]
	s_waitcnt vmcnt(8) lgkmcnt(0)
	s_barrier
	v_mfma_i32_16x16x64_i8 v[88:91], v[16:19], v[60:63], v[88:91]
	v_mfma_i32_16x16x64_i8 v[200:203], v[8:11], v[136:139], v[88:91]
	v_mfma_i32_16x16x64_i8 v[88:91], v[4:7], v[60:63], v[124:127]
	v_mfma_i32_16x16x64_i8 v[196:199], v[0:3], v[136:139], v[88:91]
	v_mfma_i32_16x16x64_i8 v[88:91], v[16:19], v[140:143], v[168:171]
	v_mfma_i32_16x16x64_i8 v[184:187], v[8:11], v[152:155], v[88:91]
	v_mfma_i32_16x16x64_i8 v[88:91], v[4:7], v[140:143], v[180:183]
	v_mfma_i32_16x16x64_i8 v[180:183], v[0:3], v[152:155], v[88:91]
	v_mfma_i32_16x16x64_i8 v[88:91], v[16:19], v[204:207], v[164:167]
	v_mfma_i32_16x16x64_i8 v[164:167], v[8:11], v[208:211], v[88:91]
	v_mfma_i32_16x16x64_i8 v[88:91], v[4:7], v[204:207], v[160:163]
	v_mfma_i32_16x16x64_i8 v[160:163], v[0:3], v[208:211], v[88:91]
	v_mfma_i32_16x16x64_i8 v[88:91], v[16:19], v[214:217], v[148:151]
	v_mfma_i32_16x16x64_i8 v[148:151], v[8:11], v[232:235], v[88:91]
	v_mfma_i32_16x16x64_i8 v[88:91], v[4:7], v[214:217], v[144:147]
	v_mfma_i32_16x16x64_i8 v[144:147], v[0:3], v[232:235], v[88:91]
	v_mfma_i32_16x16x64_i8 v[32:35], v[20:23], v[60:63], v[32:35]
	v_mfma_i32_16x16x64_i8 v[188:191], v[12:15], v[136:139], v[32:35]
	v_mfma_i32_16x16x64_i8 v[32:35], v[28:31], v[140:143], v[36:39]
	v_mfma_i32_16x16x64_i8 v[176:179], v[24:27], v[152:155], v[32:35]
	v_mfma_i32_16x16x64_i8 v[32:35], v[20:23], v[140:143], v[40:43]
	v_mfma_i32_16x16x64_i8 v[172:175], v[12:15], v[152:155], v[32:35]
	v_mfma_i32_16x16x64_i8 v[32:35], v[28:31], v[204:207], v[44:47]
	v_mfma_i32_16x16x64_i8 v[156:159], v[24:27], v[208:211], v[32:35]
	v_mfma_i32_16x16x64_i8 v[32:35], v[20:23], v[204:207], v[48:51]
	v_mfma_i32_16x16x64_i8 v[152:155], v[12:15], v[208:211], v[32:35]
	v_mfma_i32_16x16x64_i8 v[32:35], v[28:31], v[214:217], v[52:55]
	v_mfma_i32_16x16x64_i8 v[88:91], v[28:31], v[60:63], v[192:195]
	v_mfma_i32_16x16x64_i8 v[140:143], v[24:27], v[232:235], v[32:35]
	v_mfma_i32_16x16x64_i8 v[32:35], v[20:23], v[214:217], v[56:59]
	v_mfma_i32_16x16x64_i8 v[192:195], v[24:27], v[136:139], v[88:91]
	v_mfma_i32_16x16x64_i8 v[136:139], v[12:15], v[232:235], v[32:35]
	s_barrier
	ds_read_b128 v[60:63], v228 offset:49152
	ds_read_b128 v[56:59], v228 offset:50176
	ds_read_b128 v[52:55], v228 offset:51200
	ds_read_b128 v[48:51], v228 offset:52224
	ds_read_b128 v[44:47], v228 offset:53248
	ds_read_b128 v[40:43], v228 offset:54272
	ds_read_b128 v[36:39], v228 offset:55296
	ds_read_b128 v[32:35], v228 offset:56320
	s_add_i32 m0, s31, 0x18000
	s_nop 0
	global_load_lds_dwordx4 v220, s[52:53]
	s_add_i32 m0, s31, 0x1a000
	s_nop 0
	global_load_lds_dwordx4 v222, s[52:53]
	s_add_u32 s46, s50, 0x40080
	s_addc_u32 s47, s51, 0
	s_add_i32 m0, s31, 0x1c000
	s_nop 0
	global_load_lds_dwordx4 v220, s[46:47]
	s_add_i32 m0, s31, 0x1e000
	s_nop 0
	global_load_lds_dwordx4 v222, s[46:47]
	s_add_i32 m0, s31, 0x8000
	s_nop 0
	global_load_lds_dwordx4 v219, s[48:49]
	s_add_i32 m0, s31, 0xa000
	s_nop 0
	global_load_lds_dwordx4 v221, s[48:49]
	s_add_i32 s37, s37, 2
	s_add_u32 s79, s79, 0x100
	s_addc_u32 s80, s80, 0
	s_cmp_gt_u32 s37, 13
	s_waitcnt vmcnt(8) lgkmcnt(0)
	s_barrier
	v_mfma_i32_16x16x64_i8 v[88:91], v[16:19], v[60:63], v[132:135]
	v_mfma_i32_16x16x64_i8 v[132:135], v[8:11], v[56:59], v[88:91]
	v_mfma_i32_16x16x64_i8 v[88:91], v[4:7], v[60:63], v[128:131]
	v_mfma_i32_16x16x64_i8 v[128:131], v[0:3], v[56:59], v[88:91]
	v_mfma_i32_16x16x64_i8 v[88:91], v[16:19], v[52:55], v[112:115]
	v_mfma_i32_16x16x64_i8 v[112:115], v[8:11], v[48:51], v[88:91]
	v_mfma_i32_16x16x64_i8 v[88:91], v[4:7], v[52:55], v[108:111]
	v_mfma_i32_16x16x64_i8 v[108:111], v[0:3], v[48:51], v[88:91]
	v_mfma_i32_16x16x64_i8 v[88:91], v[16:19], v[44:47], v[96:99]
	v_mfma_i32_16x16x64_i8 v[96:99], v[8:11], v[40:43], v[88:91]
	v_mfma_i32_16x16x64_i8 v[88:91], v[4:7], v[44:47], v[92:95]
	v_mfma_i32_16x16x64_i8 v[76:79], v[16:19], v[36:39], v[76:79]
	v_mfma_i32_16x16x64_i8 v[72:75], v[4:7], v[36:39], v[72:75]
	v_mfma_i32_16x16x64_i8 v[92:95], v[0:3], v[40:43], v[88:91]
	v_mfma_i32_16x16x64_i8 v[76:79], v[8:11], v[32:35], v[76:79]
	v_mfma_i32_16x16x64_i8 v[72:75], v[0:3], v[32:35], v[72:75]
	v_mfma_i32_16x16x64_i8 v[88:91], v[28:31], v[60:63], v[120:123]
	v_mfma_i32_16x16x64_i8 v[120:123], v[24:27], v[56:59], v[88:91]
	v_mfma_i32_16x16x64_i8 v[88:91], v[20:23], v[60:63], v[116:119]
	v_mfma_i32_16x16x64_i8 v[116:119], v[12:15], v[56:59], v[88:91]
	v_mfma_i32_16x16x64_i8 v[88:91], v[28:31], v[52:55], v[104:107]
	v_mfma_i32_16x16x64_i8 v[104:107], v[24:27], v[48:51], v[88:91]
	v_mfma_i32_16x16x64_i8 v[88:91], v[20:23], v[52:55], v[100:103]
	v_mfma_i32_16x16x64_i8 v[84:87], v[28:31], v[44:47], v[84:87]
	v_mfma_i32_16x16x64_i8 v[80:83], v[20:23], v[44:47], v[80:83]
	v_mfma_i32_16x16x64_i8 v[68:71], v[28:31], v[36:39], v[68:71]
	v_mfma_i32_16x16x64_i8 v[64:67], v[20:23], v[36:39], v[64:67]
	v_mfma_i32_16x16x64_i8 v[100:103], v[12:15], v[48:51], v[88:91]
	v_mfma_i32_16x16x64_i8 v[84:87], v[24:27], v[40:43], v[84:87]
	v_mfma_i32_16x16x64_i8 v[80:83], v[12:15], v[40:43], v[80:83]
	v_mfma_i32_16x16x64_i8 v[68:71], v[24:27], v[32:35], v[68:71]
	v_mfma_i32_16x16x64_i8 v[64:67], v[12:15], v[32:35], v[64:67]
	s_barrier
	s_cbranch_scc1 .LBB0_935
	s_mov_b64 s[46:47], s[42:43]
	s_branch .LBB0_931

.LBB0_1410:
	s_lshl_b64 s[20:21], s[16:17], 19
	s_add_u32 s20, s39, s20
	s_addc_u32 s21, s40, s21
	s_and_b64 s[6:7], exec, s[6:7]
	s_cselect_b32 s2, s21, s29
	s_cselect_b32 s15, s20, s28
	s_add_u32 s6, s28, 0x100
	s_addc_u32 s7, s29, 0
	s_add_u32 s36, s26, 0x100
	s_addc_u32 s37, s27, 0
	s_add_u32 s30, s28, 0x180
	s_addc_u32 s31, s29, 0
	s_add_u32 s34, s26, 0x180
	s_addc_u32 s35, s27, 0
	s_add_u32 s54, s28, 0x40080
	s_addc_u32 s55, s29, 0
	s_add_i32 m0, s47, 0xc000
	s_nop 0
	global_load_lds_dwordx4 v134, s[54:55]
	s_add_i32 m0, s47, 0xe000
	s_nop 0
	global_load_lds_dwordx4 v136, s[54:55]
	s_waitcnt vmcnt(8) lgkmcnt(0)
	s_barrier
	v_mfma_f32_16x16x128_f8f6f4 v[64:67], v[0:7], v[32:39], 0
	v_mfma_f32_16x16x128_f8f6f4 v[68:71], v[8:15], v[32:39], 0
	v_mfma_f32_16x16x128_f8f6f4 v[76:79], v[8:15], v[40:47], 0
	v_mfma_f32_16x16x128_f8f6f4 v[72:75], v[0:7], v[40:47], 0
	v_mfma_f32_16x16x128_f8f6f4 v[80:83], v[0:7], v[48:55], 0
	v_mfma_f32_16x16x128_f8f6f4 v[88:91], v[8:15], v[48:55], 0
	v_mfma_f32_16x16x128_f8f6f4 v[104:107], v[8:15], v[56:63], 0
	v_mfma_f32_16x16x128_f8f6f4 v[92:95], v[0:7], v[56:63], 0
	v_mfma_f32_16x16x128_f8f6f4 v[108:111], v[16:23], v[32:39], 0
	v_mfma_f32_16x16x128_f8f6f4 v[124:127], v[24:31], v[32:39], 0
	v_mfma_f32_16x16x128_f8f6f4 v[166:169], v[24:31], v[40:47], 0
	v_mfma_f32_16x16x128_f8f6f4 v[162:165], v[16:23], v[40:47], 0
	v_mfma_f32_16x16x128_f8f6f4 v[170:173], v[16:23], v[48:55], 0
	v_mfma_f32_16x16x128_f8f6f4 v[174:177], v[24:31], v[48:55], 0
	v_mfma_f32_16x16x128_f8f6f4 v[182:185], v[24:31], v[56:63], 0
	v_mfma_f32_16x16x128_f8f6f4 v[178:181], v[16:23], v[56:63], 0
	s_barrier
	ds_read_b128 v[32:35], v140 offset:16384
	ds_read_b128 v[36:39], v140 offset:17408
	ds_read_b128 v[40:43], v140 offset:18432
	ds_read_b128 v[44:47], v140 offset:19456
	ds_read_b128 v[48:51], v140 offset:20480
	ds_read_b128 v[52:55], v140 offset:21504
	ds_read_b128 v[56:59], v140 offset:22528
	ds_read_b128 v[60:63], v140 offset:23552
	s_add_i32 m0, s47, 0x10000
	s_nop 0
	global_load_lds_dwordx4 v135, s[36:37]
	s_add_i32 m0, s47, 0x12000
	s_nop 0
	global_load_lds_dwordx4 v137, s[36:37]
	s_add_u32 s36, s26, 0x40100
	s_addc_u32 s37, s27, 0
	s_add_i32 m0, s47, 0x14000
	s_nop 0
	global_load_lds_dwordx4 v135, s[36:37]
	s_add_i32 m0, s47, 0x16000
	s_nop 0
	global_load_lds_dwordx4 v137, s[36:37]
	s_add_i32 m0, s47, 0
	s_nop 0
	global_load_lds_dwordx4 v134, s[6:7]
	s_add_i32 m0, s47, 0x2000
	s_nop 0
	global_load_lds_dwordx4 v136, s[6:7]
	s_waitcnt vmcnt(8) lgkmcnt(0)
	s_barrier
	v_mfma_f32_16x16x128_f8f6f4 v[186:189], v[0:7], v[32:39], 0
	v_mfma_f32_16x16x128_f8f6f4 v[190:193], v[8:15], v[32:39], 0
	v_mfma_f32_16x16x128_f8f6f4 v[198:201], v[8:15], v[40:47], 0
	v_mfma_f32_16x16x128_f8f6f4 v[194:197], v[0:7], v[40:47], 0
	v_mfma_f32_16x16x128_f8f6f4 v[202:205], v[0:7], v[48:55], 0
	v_mfma_f32_16x16x128_f8f6f4 v[206:209], v[8:15], v[48:55], 0
	v_mfma_f32_16x16x128_f8f6f4 v[214:217], v[8:15], v[56:63], 0
	v_mfma_f32_16x16x128_f8f6f4 v[210:213], v[0:7], v[56:63], 0
	v_mfma_f32_16x16x128_f8f6f4 v[218:221], v[16:23], v[32:39], 0
	v_mfma_f32_16x16x128_f8f6f4 v[222:225], v[24:31], v[32:39], 0
	v_mfma_f32_16x16x128_f8f6f4 v[230:233], v[24:31], v[40:47], 0
	v_mfma_f32_16x16x128_f8f6f4 v[226:229], v[16:23], v[40:47], 0
	v_mfma_f32_16x16x128_f8f6f4 v[234:237], v[16:23], v[48:55], 0
	v_mfma_f32_16x16x128_f8f6f4 v[238:241], v[24:31], v[48:55], 0
	v_mfma_f32_16x16x128_f8f6f4 v[246:249], v[24:31], v[56:63], 0
	v_mfma_f32_16x16x128_f8f6f4 v[242:245], v[16:23], v[56:63], 0
	s_barrier
	ds_read_b128 v[0:3], v141
	ds_read_b128 v[4:7], v141 offset:1024
	ds_read_b128 v[8:11], v141 offset:2048
	ds_read_b128 v[12:15], v141 offset:3072
	ds_read_b128 v[146:149], v142
	ds_read_b128 v[150:153], v142 offset:1024
	ds_read_b128 v[154:157], v142 offset:2048
	ds_read_b128 v[158:161], v142 offset:3072
	ds_read_b128 v[16:19], v140 offset:32768
	ds_read_b128 v[20:23], v140 offset:33792
	ds_read_b128 v[24:27], v140 offset:34816
	ds_read_b128 v[28:31], v140 offset:35840
	ds_read_b128 v[32:35], v140 offset:36864
	ds_read_b128 v[36:39], v140 offset:37888
	ds_read_b128 v[40:43], v140 offset:38912
	ds_read_b128 v[44:47], v140 offset:39936
	s_add_u32 s28, s28, 0x40100
	s_addc_u32 s29, s29, 0
	s_add_i32 m0, s47, 0x4000
	s_nop 0
	global_load_lds_dwordx4 v134, s[28:29]
	s_add_i32 m0, s47, 0x6000
	s_nop 0
	global_load_lds_dwordx4 v136, s[28:29]
	s_waitcnt vmcnt(8) lgkmcnt(0)
	s_barrier
	v_mfma_f32_16x16x128_f8f6f4 v[112:115], v[0:7], v[16:23], v[64:67]
	v_mfma_f32_16x16x128_f8f6f4 v[116:119], v[8:15], v[16:23], v[68:71]
	v_mfma_f32_16x16x128_f8f6f4 v[100:103], v[0:7], v[24:31], v[72:75]
	v_mfma_f32_16x16x128_f8f6f4 v[96:99], v[8:15], v[24:31], v[76:79]
	v_mfma_f32_16x16x128_f8f6f4 v[84:87], v[0:7], v[32:39], v[80:83]
	v_mfma_f32_16x16x128_f8f6f4 v[80:83], v[8:15], v[32:39], v[88:91]
	v_mfma_f32_16x16x128_f8f6f4 v[60:63], v[0:7], v[40:47], v[92:95]
	v_mfma_f32_16x16x128_f8f6f4 v[56:59], v[8:15], v[40:47], v[104:107]
	v_mfma_f32_16x16x128_f8f6f4 v[120:123], v[146:153], v[16:23], v[108:111]
	v_mfma_f32_16x16x128_f8f6f4 v[124:127], v[154:161], v[16:23], v[124:127]
	v_mfma_f32_16x16x128_f8f6f4 v[108:111], v[146:153], v[24:31], v[162:165]
	v_mfma_f32_16x16x128_f8f6f4 v[104:107], v[154:161], v[24:31], v[166:169]
	v_mfma_f32_16x16x128_f8f6f4 v[92:95], v[146:153], v[32:39], v[170:173]
	v_mfma_f32_16x16x128_f8f6f4 v[88:91], v[154:161], v[32:39], v[174:177]
	v_mfma_f32_16x16x128_f8f6f4 v[76:79], v[146:153], v[40:47], v[178:181]
	v_mfma_f32_16x16x128_f8f6f4 v[72:75], v[154:161], v[40:47], v[182:185]
	s_barrier
	ds_read_b128 v[24:27], v140 offset:49152
	ds_read_b128 v[28:31], v140 offset:50176
	ds_read_b128 v[162:165], v140 offset:51200
	ds_read_b128 v[166:169], v140 offset:52224
	ds_read_b128 v[170:173], v140 offset:53248
	ds_read_b128 v[174:177], v140 offset:54272
	ds_read_b128 v[178:181], v140 offset:55296
	ds_read_b128 v[182:185], v140 offset:56320
	s_add_i32 m0, s47, 0x18000
	s_nop 0
	global_load_lds_dwordx4 v135, s[34:35]
	s_add_i32 m0, s47, 0x1a000
	s_nop 0
	global_load_lds_dwordx4 v137, s[34:35]
	s_add_u32 s28, s26, 0x40180
	s_addc_u32 s29, s27, 0
	s_add_i32 m0, s47, 0x1c000
	s_nop 0
	global_load_lds_dwordx4 v135, s[28:29]
	s_add_i32 m0, s47, 0x1e000
	s_nop 0
	global_load_lds_dwordx4 v137, s[28:29]
	s_add_i32 m0, s47, 0x8000
	s_nop 0
	global_load_lds_dwordx4 v134, s[30:31]
	s_add_i32 m0, s47, 0xa000
	s_nop 0
	global_load_lds_dwordx4 v136, s[30:31]
	s_waitcnt vmcnt(8) lgkmcnt(0)
	s_barrier
	v_mfma_f32_16x16x128_f8f6f4 v[52:55], v[0:7], v[24:31], v[186:189]
	v_mfma_f32_16x16x128_f8f6f4 v[48:51], v[8:15], v[24:31], v[190:193]
	v_mfma_f32_16x16x128_f8f6f4 v[36:39], v[0:7], v[162:169], v[194:197]
	v_mfma_f32_16x16x128_f8f6f4 v[32:35], v[8:15], v[162:169], v[198:201]
	v_mfma_f32_16x16x128_f8f6f4 v[20:23], v[0:7], v[170:177], v[202:205]
	v_mfma_f32_16x16x128_f8f6f4 v[16:19], v[8:15], v[170:177], v[206:209]
	v_mfma_f32_16x16x128_f8f6f4 v[4:7], v[0:7], v[178:185], v[210:213]
	v_mfma_f32_16x16x128_f8f6f4 v[0:3], v[8:15], v[178:185], v[214:217]
	v_mfma_f32_16x16x128_f8f6f4 v[68:71], v[146:153], v[24:31], v[218:221]
	v_mfma_f32_16x16x128_f8f6f4 v[64:67], v[154:161], v[24:31], v[222:225]
	v_mfma_f32_16x16x128_f8f6f4 v[44:47], v[146:153], v[162:169], v[226:229]
	v_mfma_f32_16x16x128_f8f6f4 v[40:43], v[154:161], v[162:169], v[230:233]
	v_mfma_f32_16x16x128_f8f6f4 v[28:31], v[146:153], v[170:177], v[234:237]
	v_mfma_f32_16x16x128_f8f6f4 v[24:27], v[154:161], v[170:177], v[238:241]
	v_mfma_f32_16x16x128_f8f6f4 v[12:15], v[146:153], v[178:185], v[242:245]
	v_mfma_f32_16x16x128_f8f6f4 v[8:11], v[154:161], v[178:185], v[246:249]
	s_barrier
	s_add_u32 s17, s26, 0x200
	s_addc_u32 s54, s27, 0
	s_mov_b32 s55, 0
.LBB0_1411:
	ds_read_b128 v[146:149], v138
	ds_read_b128 v[150:153], v138 offset:1024
	ds_read_b128 v[154:157], v138 offset:2048
	ds_read_b128 v[158:161], v138 offset:3072
	ds_read_b128 v[162:165], v139
	ds_read_b128 v[166:169], v139 offset:1024
	ds_read_b128 v[170:173], v139 offset:2048
	ds_read_b128 v[174:177], v139 offset:3072
	ds_read_b128 v[178:181], v140
	ds_read_b128 v[182:185], v140 offset:1024
	ds_read_b128 v[186:189], v140 offset:2048
	ds_read_b128 v[190:193], v140 offset:3072
	ds_read_b128 v[194:197], v140 offset:4096
	ds_read_b128 v[198:201], v140 offset:5120
	ds_read_b128 v[202:205], v140 offset:6144
	ds_read_b128 v[206:209], v140 offset:7168
	s_add_u32 s26, s6, 0x100
	s_addc_u32 s27, s7, 0
	s_cmp_eq_u32 s55, 12
	s_cselect_b32 s36, s15, s26
	s_cselect_b32 s37, s2, s27
	s_cselect_b32 s30, s18, s17
	s_cselect_b32 s31, s19, s54
	s_add_u32 s28, s36, 0x80
	s_addc_u32 s29, s37, 0
	s_add_u32 s34, s30, 0x80
	s_addc_u32 s35, s31, 0
	s_add_u32 s6, s6, 0x40080
	s_addc_u32 s7, s7, 0
	s_add_i32 m0, s47, 0xc000
	s_nop 0
	global_load_lds_dwordx4 v134, s[6:7]
	s_add_i32 m0, s47, 0xe000
	s_nop 0
	global_load_lds_dwordx4 v136, s[6:7]
	s_waitcnt vmcnt(8) lgkmcnt(0)
	s_barrier
	v_mfma_f32_16x16x128_f8f6f4 v[112:115], v[146:153], v[178:185], v[112:115]
	v_mfma_f32_16x16x128_f8f6f4 v[116:119], v[154:161], v[178:185], v[116:119]
	v_mfma_f32_16x16x128_f8f6f4 v[96:99], v[154:161], v[186:193], v[96:99]
	v_mfma_f32_16x16x128_f8f6f4 v[100:103], v[146:153], v[186:193], v[100:103]
	v_mfma_f32_16x16x128_f8f6f4 v[210:213], v[146:153], v[194:201], v[84:87]
	v_mfma_f32_16x16x128_f8f6f4 v[214:217], v[154:161], v[194:201], v[80:83]
	v_mfma_f32_16x16x128_f8f6f4 v[222:225], v[154:161], v[202:209], v[56:59]
	v_mfma_f32_16x16x128_f8f6f4 v[218:221], v[146:153], v[202:209], v[60:63]
	v_mfma_f32_16x16x128_f8f6f4 v[120:123], v[162:169], v[178:185], v[120:123]
	v_mfma_f32_16x16x128_f8f6f4 v[124:127], v[170:177], v[178:185], v[124:127]
	v_mfma_f32_16x16x128_f8f6f4 v[108:111], v[162:169], v[186:193], v[108:111]
	v_mfma_f32_16x16x128_f8f6f4 v[104:107], v[170:177], v[186:193], v[104:107]
	v_mfma_f32_16x16x128_f8f6f4 v[178:181], v[162:169], v[194:201], v[92:95]
	v_mfma_f32_16x16x128_f8f6f4 v[182:185], v[170:177], v[194:201], v[88:91]
	v_mfma_f32_16x16x128_f8f6f4 v[186:189], v[162:169], v[202:209], v[76:79]
	v_mfma_f32_16x16x128_f8f6f4 v[190:193], v[170:177], v[202:209], v[72:75]
	s_barrier
	ds_read_b128 v[56:59], v140 offset:16384
	ds_read_b128 v[60:63], v140 offset:17408
	s_nop 2
	ds_read_b128 v[72:75], v140 offset:18432
	ds_read_b128 v[76:79], v140 offset:19456
	ds_read_b128 v[80:83], v140 offset:20480
	ds_read_b128 v[84:87], v140 offset:21504
	ds_read_b128 v[88:91], v140 offset:22528
	ds_read_b128 v[92:95], v140 offset:23552
	s_add_i32 m0, s47, 0x10000
	s_nop 0
	global_load_lds_dwordx4 v135, s[30:31]
	s_add_i32 m0, s47, 0x12000
	s_nop 0
	global_load_lds_dwordx4 v137, s[30:31]
	s_add_u32 s6, s30, 0x40000
	s_addc_u32 s7, s31, 0
	s_add_i32 m0, s47, 0x14000
	s_nop 0
	global_load_lds_dwordx4 v135, s[6:7]
	s_add_i32 m0, s47, 0x16000
	s_nop 0
	global_load_lds_dwordx4 v137, s[6:7]
	s_add_i32 m0, s47, 0
	s_nop 0
	global_load_lds_dwordx4 v134, s[36:37]
	s_add_i32 m0, s47, 0x2000
	s_nop 0
	global_load_lds_dwordx4 v136, s[36:37]
	s_waitcnt vmcnt(8) lgkmcnt(0)
	s_barrier
	v_mfma_f32_16x16x128_f8f6f4 v[52:55], v[146:153], v[56:63], v[52:55]
	v_mfma_f32_16x16x128_f8f6f4 v[48:51], v[154:161], v[56:63], v[48:51]
	v_mfma_f32_16x16x128_f8f6f4 v[198:201], v[154:161], v[72:79], v[32:35]
	v_mfma_f32_16x16x128_f8f6f4 v[194:197], v[146:153], v[72:79], v[36:39]
	v_mfma_f32_16x16x128_f8f6f4 v[202:205], v[146:153], v[80:87], v[20:23]
	v_mfma_f32_16x16x128_f8f6f4 v[206:209], v[154:161], v[80:87], v[16:19]
	v_mfma_f32_16x16x128_f8f6f4 v[230:233], v[154:161], v[88:95], v[0:3]
	v_mfma_f32_16x16x128_f8f6f4 v[226:229], v[146:153], v[88:95], v[4:7]
	v_mfma_f32_16x16x128_f8f6f4 v[68:71], v[162:169], v[56:63], v[68:71]
	v_mfma_f32_16x16x128_f8f6f4 v[64:67], v[170:177], v[56:63], v[64:67]
	v_mfma_f32_16x16x128_f8f6f4 v[238:241], v[170:177], v[72:79], v[40:43]
	v_mfma_f32_16x16x128_f8f6f4 v[234:237], v[162:169], v[72:79], v[44:47]
	v_mfma_f32_16x16x128_f8f6f4 v[242:245], v[162:169], v[80:87], v[28:31]
	v_mfma_f32_16x16x128_f8f6f4 v[246:249], v[170:177], v[80:87], v[24:27]
	v_mfma_f32_16x16x128_f8f6f4 v[130:133], v[170:177], v[88:95], v[8:11]
	v_mfma_f32_16x16x128_f8f6f4 v[250:253], v[162:169], v[88:95], v[12:15]
	s_barrier
	ds_read_b128 v[0:3], v141
	ds_read_b128 v[4:7], v141 offset:1024
	s_nop 2
	ds_read_b128 v[8:11], v141 offset:2048
	ds_read_b128 v[12:15], v141 offset:3072
	ds_read_b128 v[146:149], v142
	ds_read_b128 v[150:153], v142 offset:1024
	ds_read_b128 v[154:157], v142 offset:2048
	ds_read_b128 v[158:161], v142 offset:3072
	ds_read_b128 v[16:19], v140 offset:32768
	ds_read_b128 v[20:23], v140 offset:33792
	ds_read_b128 v[24:27], v140 offset:34816
	ds_read_b128 v[28:31], v140 offset:35840
	ds_read_b128 v[32:35], v140 offset:36864
	ds_read_b128 v[36:39], v140 offset:37888
	ds_read_b128 v[40:43], v140 offset:38912
	ds_read_b128 v[44:47], v140 offset:39936
	s_add_u32 s6, s36, 0x40000
	s_addc_u32 s7, s37, 0
	s_add_i32 m0, s47, 0x4000
	s_nop 0
	global_load_lds_dwordx4 v134, s[6:7]
	s_add_i32 m0, s47, 0x6000
	s_nop 0
	global_load_lds_dwordx4 v136, s[6:7]
	s_waitcnt vmcnt(8) lgkmcnt(0)
	s_barrier
	v_mfma_f32_16x16x128_f8f6f4 v[112:115], v[0:7], v[16:23], v[112:115]
	v_mfma_f32_16x16x128_f8f6f4 v[116:119], v[8:15], v[16:23], v[116:119]
	v_mfma_f32_16x16x128_f8f6f4 v[96:99], v[8:15], v[24:31], v[96:99]
	v_mfma_f32_16x16x128_f8f6f4 v[100:103], v[0:7], v[24:31], v[100:103]
	v_mfma_f32_16x16x128_f8f6f4 v[84:87], v[0:7], v[32:39], v[210:213]
	v_mfma_f32_16x16x128_f8f6f4 v[80:83], v[8:15], v[32:39], v[214:217]
	v_mfma_f32_16x16x128_f8f6f4 v[56:59], v[8:15], v[40:47], v[222:225]
	v_mfma_f32_16x16x128_f8f6f4 v[60:63], v[0:7], v[40:47], v[218:221]
	v_mfma_f32_16x16x128_f8f6f4 v[120:123], v[146:153], v[16:23], v[120:123]
	v_mfma_f32_16x16x128_f8f6f4 v[124:127], v[154:161], v[16:23], v[124:127]
	v_mfma_f32_16x16x128_f8f6f4 v[104:107], v[154:161], v[24:31], v[104:107]
	v_mfma_f32_16x16x128_f8f6f4 v[108:111], v[146:153], v[24:31], v[108:111]
	v_mfma_f32_16x16x128_f8f6f4 v[92:95], v[146:153], v[32:39], v[178:181]
	v_mfma_f32_16x16x128_f8f6f4 v[88:91], v[154:161], v[32:39], v[182:185]
	v_mfma_f32_16x16x128_f8f6f4 v[72:75], v[154:161], v[40:47], v[190:193]
	v_mfma_f32_16x16x128_f8f6f4 v[76:79], v[146:153], v[40:47], v[186:189]
	s_barrier
	ds_read_b128 v[24:27], v140 offset:49152
	ds_read_b128 v[28:31], v140 offset:50176
	ds_read_b128 v[162:165], v140 offset:51200
	ds_read_b128 v[166:169], v140 offset:52224
	ds_read_b128 v[170:173], v140 offset:53248
	ds_read_b128 v[174:177], v140 offset:54272
	ds_read_b128 v[178:181], v140 offset:55296
	ds_read_b128 v[182:185], v140 offset:56320
	s_add_i32 m0, s47, 0x18000
	s_nop 0
	global_load_lds_dwordx4 v135, s[34:35]
	s_add_i32 m0, s47, 0x1a000
	s_nop 0
	global_load_lds_dwordx4 v137, s[34:35]
	s_add_u32 s6, s30, 0x40080
	s_addc_u32 s7, s31, 0
	s_add_i32 m0, s47, 0x1c000
	s_nop 0
	global_load_lds_dwordx4 v135, s[6:7]
	s_add_i32 m0, s47, 0x1e000
	s_nop 0
	global_load_lds_dwordx4 v137, s[6:7]
	s_add_i32 m0, s47, 0x8000
	s_nop 0
	global_load_lds_dwordx4 v134, s[28:29]
	s_add_i32 m0, s47, 0xa000
	s_nop 0
	global_load_lds_dwordx4 v136, s[28:29]
	s_add_i32 s55, s55, 2
	s_add_u32 s17, s17, 0x100
	s_addc_u32 s54, s54, 0
	s_cmp_gt_u32 s55, 13
	s_mov_b64 s[6:7], s[26:27]
	s_waitcnt vmcnt(8) lgkmcnt(0)
	s_barrier
	v_mfma_f32_16x16x128_f8f6f4 v[52:55], v[0:7], v[24:31], v[52:55]
	v_mfma_f32_16x16x128_f8f6f4 v[48:51], v[8:15], v[24:31], v[48:51]
	v_mfma_f32_16x16x128_f8f6f4 v[36:39], v[0:7], v[162:169], v[194:197]
	v_mfma_f32_16x16x128_f8f6f4 v[32:35], v[8:15], v[162:169], v[198:201]
	v_mfma_f32_16x16x128_f8f6f4 v[20:23], v[0:7], v[170:177], v[202:205]
	v_mfma_f32_16x16x128_f8f6f4 v[16:19], v[8:15], v[170:177], v[206:209]
	v_mfma_f32_16x16x128_f8f6f4 v[4:7], v[0:7], v[178:185], v[226:229]
	v_mfma_f32_16x16x128_f8f6f4 v[0:3], v[8:15], v[178:185], v[230:233]
	v_mfma_f32_16x16x128_f8f6f4 v[68:71], v[146:153], v[24:31], v[68:71]
	v_mfma_f32_16x16x128_f8f6f4 v[64:67], v[154:161], v[24:31], v[64:67]
	v_mfma_f32_16x16x128_f8f6f4 v[44:47], v[146:153], v[162:169], v[234:237]
	v_mfma_f32_16x16x128_f8f6f4 v[40:43], v[154:161], v[162:169], v[238:241]
	v_mfma_f32_16x16x128_f8f6f4 v[28:31], v[146:153], v[170:177], v[242:245]
	v_mfma_f32_16x16x128_f8f6f4 v[24:27], v[154:161], v[170:177], v[246:249]
	v_mfma_f32_16x16x128_f8f6f4 v[12:15], v[146:153], v[178:185], v[250:253]
	v_mfma_f32_16x16x128_f8f6f4 v[8:11], v[154:161], v[178:185], v[130:133]
	s_barrier
	s_cbranch_scc0 .LBB0_1411
	s_and_b64 vcc, exec, s[12:13]
	s_cbranch_vccz .LBB0_1414
	s_barrier

.LBB0_1487:
	s_add_u32 s26, s28, 0x100
	s_addc_u32 s27, s29, 0
	s_add_u32 s36, s24, 0x100
	s_addc_u32 s37, s25, 0
	s_add_u32 s30, s28, 0x180
	s_addc_u32 s31, s29, 0
	s_add_u32 s34, s24, 0x180
	s_addc_u32 s35, s25, 0
	s_add_u32 s52, s28, 0xe0080
	s_addc_u32 s53, s29, 0
	s_add_i32 m0, s44, 0xc000
	s_nop 0
	global_load_lds_dwordx4 v149, s[52:53]
	s_add_i32 m0, s44, 0xe000
	s_nop 0
	global_load_lds_dwordx4 v151, s[52:53]
	s_waitcnt vmcnt(8) lgkmcnt(0)
	s_barrier
	v_mfma_f32_16x16x128_f8f6f4 v[64:67], v[0:7], v[32:39], 0
	v_mfma_f32_16x16x128_f8f6f4 v[68:71], v[8:15], v[32:39], 0
	v_mfma_f32_16x16x128_f8f6f4 v[76:79], v[8:15], v[40:47], 0
	v_mfma_f32_16x16x128_f8f6f4 v[72:75], v[0:7], v[40:47], 0
	v_mfma_f32_16x16x128_f8f6f4 v[80:83], v[0:7], v[48:55], 0
	v_mfma_f32_16x16x128_f8f6f4 v[88:91], v[8:15], v[48:55], 0
	v_mfma_f32_16x16x128_f8f6f4 v[104:107], v[8:15], v[56:63], 0
	v_mfma_f32_16x16x128_f8f6f4 v[92:95], v[0:7], v[56:63], 0
	v_mfma_f32_16x16x128_f8f6f4 v[108:111], v[16:23], v[32:39], 0
	v_mfma_f32_16x16x128_f8f6f4 v[124:127], v[24:31], v[32:39], 0
	v_mfma_f32_16x16x128_f8f6f4 v[162:165], v[24:31], v[40:47], 0
	v_mfma_f32_16x16x128_f8f6f4 v[158:161], v[16:23], v[40:47], 0
	v_mfma_f32_16x16x128_f8f6f4 v[166:169], v[16:23], v[48:55], 0
	v_mfma_f32_16x16x128_f8f6f4 v[170:173], v[24:31], v[48:55], 0
	v_mfma_f32_16x16x128_f8f6f4 v[178:181], v[24:31], v[56:63], 0
	v_mfma_f32_16x16x128_f8f6f4 v[174:177], v[16:23], v[56:63], 0
	s_barrier
	ds_read_b128 v[32:35], v155 offset:16384
	ds_read_b128 v[36:39], v155 offset:17408
	ds_read_b128 v[40:43], v155 offset:18432
	ds_read_b128 v[44:47], v155 offset:19456
	ds_read_b128 v[48:51], v155 offset:20480
	ds_read_b128 v[52:55], v155 offset:21504
	ds_read_b128 v[56:59], v155 offset:22528
	ds_read_b128 v[60:63], v155 offset:23552
	s_add_i32 m0, s44, 0x10000
	s_nop 0
	global_load_lds_dwordx4 v150, s[36:37]
	s_add_i32 m0, s44, 0x12000
	s_nop 0
	global_load_lds_dwordx4 v152, s[36:37]
	s_add_u32 s36, s24, 0xe0100
	s_addc_u32 s37, s25, 0
	s_add_i32 m0, s44, 0x14000
	s_nop 0
	global_load_lds_dwordx4 v150, s[36:37]
	s_add_i32 m0, s44, 0x16000
	s_nop 0
	global_load_lds_dwordx4 v152, s[36:37]
	s_add_i32 m0, s44, 0
	s_nop 0
	global_load_lds_dwordx4 v149, s[26:27]
	s_add_i32 m0, s44, 0x2000
	s_nop 0
	global_load_lds_dwordx4 v151, s[26:27]
	s_waitcnt vmcnt(8) lgkmcnt(0)
	s_barrier
	v_mfma_f32_16x16x128_f8f6f4 v[190:193], v[0:7], v[32:39], 0
	v_mfma_f32_16x16x128_f8f6f4 v[194:197], v[8:15], v[32:39], 0
	v_mfma_f32_16x16x128_f8f6f4 v[202:205], v[8:15], v[40:47], 0
	v_mfma_f32_16x16x128_f8f6f4 v[198:201], v[0:7], v[40:47], 0
	v_mfma_f32_16x16x128_f8f6f4 v[206:209], v[0:7], v[48:55], 0
	v_mfma_f32_16x16x128_f8f6f4 v[210:213], v[8:15], v[48:55], 0
	v_mfma_f32_16x16x128_f8f6f4 v[218:221], v[8:15], v[56:63], 0
	v_mfma_f32_16x16x128_f8f6f4 v[214:217], v[0:7], v[56:63], 0
	v_mfma_f32_16x16x128_f8f6f4 v[222:225], v[16:23], v[32:39], 0
	v_mfma_f32_16x16x128_f8f6f4 v[226:229], v[24:31], v[32:39], 0
	v_mfma_f32_16x16x128_f8f6f4 v[234:237], v[24:31], v[40:47], 0
	v_mfma_f32_16x16x128_f8f6f4 v[230:233], v[16:23], v[40:47], 0
	v_mfma_f32_16x16x128_f8f6f4 v[238:241], v[16:23], v[48:55], 0
	v_mfma_f32_16x16x128_f8f6f4 v[242:245], v[24:31], v[48:55], 0
	v_mfma_f32_16x16x128_f8f6f4 v[250:253], v[24:31], v[56:63], 0
	v_mfma_f32_16x16x128_f8f6f4 v[246:249], v[16:23], v[56:63], 0
	s_barrier
	ds_read_b128 v[0:3], v156
	ds_read_b128 v[4:7], v156 offset:1024
	ds_read_b128 v[16:19], v156 offset:2048
	ds_read_b128 v[20:23], v156 offset:3072
	ds_read_b128 v[132:135], v157
	ds_read_b128 v[136:139], v157 offset:1024
	ds_read_b128 v[140:143], v157 offset:2048
	ds_read_b128 v[144:147], v157 offset:3072
	ds_read_b128 v[8:11], v155 offset:32768
	ds_read_b128 v[12:15], v155 offset:33792
	ds_read_b128 v[24:27], v155 offset:34816
	ds_read_b128 v[28:31], v155 offset:35840
	ds_read_b128 v[32:35], v155 offset:36864
	ds_read_b128 v[36:39], v155 offset:37888
	ds_read_b128 v[40:43], v155 offset:38912
	ds_read_b128 v[44:47], v155 offset:39936
	s_add_u32 s28, s28, 0xe0100
	s_addc_u32 s29, s29, 0
	s_add_i32 m0, s44, 0x4000
	s_nop 0
	global_load_lds_dwordx4 v149, s[28:29]
	s_add_i32 m0, s44, 0x6000
	s_nop 0
	global_load_lds_dwordx4 v151, s[28:29]
	s_waitcnt vmcnt(8) lgkmcnt(0)
	s_barrier
	v_mfma_f32_16x16x128_f8f6f4 v[112:115], v[0:7], v[8:15], v[64:67]
	v_mfma_f32_16x16x128_f8f6f4 v[116:119], v[16:23], v[8:15], v[68:71]
	v_mfma_f32_16x16x128_f8f6f4 v[100:103], v[0:7], v[24:31], v[72:75]
	v_mfma_f32_16x16x128_f8f6f4 v[96:99], v[16:23], v[24:31], v[76:79]
	v_mfma_f32_16x16x128_f8f6f4 v[84:87], v[0:7], v[32:39], v[80:83]
	v_mfma_f32_16x16x128_f8f6f4 v[80:83], v[16:23], v[32:39], v[88:91]
	v_mfma_f32_16x16x128_f8f6f4 v[60:63], v[0:7], v[40:47], v[92:95]
	v_mfma_f32_16x16x128_f8f6f4 v[52:55], v[16:23], v[40:47], v[104:107]
	v_mfma_f32_16x16x128_f8f6f4 v[120:123], v[132:139], v[8:15], v[108:111]
	v_mfma_f32_16x16x128_f8f6f4 v[124:127], v[140:147], v[8:15], v[124:127]
	v_mfma_f32_16x16x128_f8f6f4 v[108:111], v[132:139], v[24:31], v[158:161]
	v_mfma_f32_16x16x128_f8f6f4 v[104:107], v[140:147], v[24:31], v[162:165]
	v_mfma_f32_16x16x128_f8f6f4 v[92:95], v[132:139], v[32:39], v[166:169]
	v_mfma_f32_16x16x128_f8f6f4 v[88:91], v[140:147], v[32:39], v[170:173]
	v_mfma_f32_16x16x128_f8f6f4 v[56:59], v[132:139], v[40:47], v[174:177]
	v_mfma_f32_16x16x128_f8f6f4 v[48:51], v[140:147], v[40:47], v[178:181]
	s_barrier
	ds_read_b128 v[158:161], v155 offset:49152
	ds_read_b128 v[162:165], v155 offset:50176
	ds_read_b128 v[166:169], v155 offset:51200
	ds_read_b128 v[170:173], v155 offset:52224
	ds_read_b128 v[174:177], v155 offset:53248
	ds_read_b128 v[178:181], v155 offset:54272
	ds_read_b128 v[182:185], v155 offset:55296
	ds_read_b128 v[186:189], v155 offset:56320
	s_add_i32 m0, s44, 0x18000
	s_nop 0
	global_load_lds_dwordx4 v150, s[34:35]
	s_add_i32 m0, s44, 0x1a000
	s_nop 0
	global_load_lds_dwordx4 v152, s[34:35]
	s_add_u32 s28, s24, 0xe0180
	s_addc_u32 s29, s25, 0
	s_add_i32 m0, s44, 0x1c000
	s_nop 0
	global_load_lds_dwordx4 v150, s[28:29]
	s_add_i32 m0, s44, 0x1e000
	s_nop 0
	global_load_lds_dwordx4 v152, s[28:29]
	s_add_i32 m0, s44, 0x8000
	s_nop 0
	global_load_lds_dwordx4 v149, s[30:31]
	s_add_i32 m0, s44, 0xa000
	s_nop 0
	global_load_lds_dwordx4 v151, s[30:31]
	s_waitcnt vmcnt(8) lgkmcnt(0)
	s_barrier
	v_mfma_f32_16x16x128_f8f6f4 v[68:71], v[0:7], v[158:165], v[190:193]
	v_mfma_f32_16x16x128_f8f6f4 v[64:67], v[16:23], v[158:165], v[194:197]
	v_mfma_f32_16x16x128_f8f6f4 v[36:39], v[16:23], v[166:173], v[202:205]
	v_mfma_f32_16x16x128_f8f6f4 v[44:47], v[0:7], v[166:173], v[198:201]
	v_mfma_f32_16x16x128_f8f6f4 v[28:31], v[0:7], v[174:181], v[206:209]
	v_mfma_f32_16x16x128_f8f6f4 v[24:27], v[16:23], v[174:181], v[210:213]
	v_mfma_f32_16x16x128_f8f6f4 v[8:11], v[16:23], v[182:189], v[218:221]
	v_mfma_f32_16x16x128_f8f6f4 v[12:15], v[0:7], v[182:189], v[214:217]
	v_mfma_f32_16x16x128_f8f6f4 v[76:79], v[132:139], v[158:165], v[222:225]
	v_mfma_f32_16x16x128_f8f6f4 v[72:75], v[140:147], v[158:165], v[226:229]
	v_mfma_f32_16x16x128_f8f6f4 v[32:35], v[140:147], v[166:173], v[234:237]
	v_mfma_f32_16x16x128_f8f6f4 v[40:43], v[132:139], v[166:173], v[230:233]
	v_mfma_f32_16x16x128_f8f6f4 v[20:23], v[132:139], v[174:181], v[238:241]
	v_mfma_f32_16x16x128_f8f6f4 v[16:19], v[140:147], v[174:181], v[242:245]
	v_mfma_f32_16x16x128_f8f6f4 v[0:3], v[140:147], v[182:189], v[250:253]
	v_mfma_f32_16x16x128_f8f6f4 v[4:7], v[132:139], v[182:189], v[246:249]
	s_barrier
	s_add_u32 s23, s24, 0x200
	s_addc_u32 s51, s25, 0
	s_mov_b32 s52, 0
.LBB0_1488:
	ds_read_b128 v[132:135], v153
	ds_read_b128 v[136:139], v153 offset:1024
	ds_read_b128 v[140:143], v153 offset:2048
	ds_read_b128 v[144:147], v153 offset:3072
	ds_read_b128 v[158:161], v154
	ds_read_b128 v[162:165], v154 offset:1024
	ds_read_b128 v[166:169], v154 offset:2048
	ds_read_b128 v[170:173], v154 offset:3072
	ds_read_b128 v[174:177], v155
	ds_read_b128 v[178:181], v155 offset:1024
	ds_read_b128 v[182:185], v155 offset:2048
	ds_read_b128 v[186:189], v155 offset:3072
	ds_read_b128 v[190:193], v155 offset:4096
	ds_read_b128 v[194:197], v155 offset:5120
	ds_read_b128 v[198:201], v155 offset:6144
	ds_read_b128 v[202:205], v155 offset:7168
	s_add_u32 s24, s26, 0x100
	s_addc_u32 s25, s27, 0
	s_cmp_eq_u32 s52, 52
	s_cselect_b32 s36, s6, s24
	s_cselect_b32 s37, s7, s25
	s_cselect_b32 s30, s20, s23
	s_cselect_b32 s31, s21, s51
	s_add_u32 s28, s36, 0x80
	s_addc_u32 s29, s37, 0
	s_add_u32 s34, s30, 0x80
	s_addc_u32 s35, s31, 0
	s_add_u32 s26, s26, 0xe0080
	s_addc_u32 s27, s27, 0
	s_add_i32 m0, s44, 0xc000
	s_nop 0
	global_load_lds_dwordx4 v149, s[26:27]
	s_add_i32 m0, s44, 0xe000
	s_nop 0
	global_load_lds_dwordx4 v151, s[26:27]
	s_waitcnt vmcnt(8) lgkmcnt(0)
	s_barrier
	v_mfma_f32_16x16x128_f8f6f4 v[112:115], v[132:139], v[174:181], v[112:115]
	v_mfma_f32_16x16x128_f8f6f4 v[116:119], v[140:147], v[174:181], v[116:119]
	v_mfma_f32_16x16x128_f8f6f4 v[96:99], v[140:147], v[182:189], v[96:99]
	v_mfma_f32_16x16x128_f8f6f4 v[100:103], v[132:139], v[182:189], v[100:103]
	v_mfma_f32_16x16x128_f8f6f4 v[206:209], v[132:139], v[190:197], v[84:87]
	v_mfma_f32_16x16x128_f8f6f4 v[210:213], v[140:147], v[190:197], v[80:83]
	v_mfma_f32_16x16x128_f8f6f4 v[218:221], v[140:147], v[198:205], v[52:55]
	v_mfma_f32_16x16x128_f8f6f4 v[214:217], v[132:139], v[198:205], v[60:63]
	v_mfma_f32_16x16x128_f8f6f4 v[120:123], v[158:165], v[174:181], v[120:123]
	v_mfma_f32_16x16x128_f8f6f4 v[124:127], v[166:173], v[174:181], v[124:127]
	v_mfma_f32_16x16x128_f8f6f4 v[108:111], v[158:165], v[182:189], v[108:111]
	v_mfma_f32_16x16x128_f8f6f4 v[104:107], v[166:173], v[182:189], v[104:107]
	v_mfma_f32_16x16x128_f8f6f4 v[174:177], v[158:165], v[190:197], v[92:95]
	v_mfma_f32_16x16x128_f8f6f4 v[178:181], v[166:173], v[190:197], v[88:91]
	v_mfma_f32_16x16x128_f8f6f4 v[182:185], v[158:165], v[198:205], v[56:59]
	v_mfma_f32_16x16x128_f8f6f4 v[186:189], v[166:173], v[198:205], v[48:51]
	s_barrier
	s_nop 4
	ds_read_b128 v[48:51], v155 offset:16384
	ds_read_b128 v[52:55], v155 offset:17408
	ds_read_b128 v[56:59], v155 offset:18432
	ds_read_b128 v[60:63], v155 offset:19456
	ds_read_b128 v[80:83], v155 offset:20480
	ds_read_b128 v[84:87], v155 offset:21504
	ds_read_b128 v[88:91], v155 offset:22528
	ds_read_b128 v[92:95], v155 offset:23552
	s_add_i32 m0, s44, 0x10000
	s_nop 0
	global_load_lds_dwordx4 v150, s[30:31]
	s_add_i32 m0, s44, 0x12000
	s_nop 0
	global_load_lds_dwordx4 v152, s[30:31]
	s_add_u32 s26, s30, 0xe0000
	s_addc_u32 s27, s31, 0
	s_add_i32 m0, s44, 0x14000
	s_nop 0
	global_load_lds_dwordx4 v150, s[26:27]
	s_add_i32 m0, s44, 0x16000
	s_nop 0
	global_load_lds_dwordx4 v152, s[26:27]
	s_add_i32 m0, s44, 0
	s_nop 0
	global_load_lds_dwordx4 v149, s[36:37]
	s_add_i32 m0, s44, 0x2000
	s_nop 0
	global_load_lds_dwordx4 v151, s[36:37]
	s_waitcnt vmcnt(8) lgkmcnt(0)
	s_barrier
	v_mfma_f32_16x16x128_f8f6f4 v[68:71], v[132:139], v[48:55], v[68:71]
	v_mfma_f32_16x16x128_f8f6f4 v[64:67], v[140:147], v[48:55], v[64:67]
	v_mfma_f32_16x16x128_f8f6f4 v[194:197], v[140:147], v[56:63], v[36:39]
	v_mfma_f32_16x16x128_f8f6f4 v[190:193], v[132:139], v[56:63], v[44:47]
	v_mfma_f32_16x16x128_f8f6f4 v[198:201], v[132:139], v[80:87], v[28:31]
	v_mfma_f32_16x16x128_f8f6f4 v[202:205], v[140:147], v[80:87], v[24:27]
	v_mfma_f32_16x16x128_f8f6f4 v[226:229], v[140:147], v[88:95], v[8:11]
	v_mfma_f32_16x16x128_f8f6f4 v[222:225], v[132:139], v[88:95], v[12:15]
	v_mfma_f32_16x16x128_f8f6f4 v[76:79], v[158:165], v[48:55], v[76:79]
	v_mfma_f32_16x16x128_f8f6f4 v[72:75], v[166:173], v[48:55], v[72:75]
	v_mfma_f32_16x16x128_f8f6f4 v[234:237], v[166:173], v[56:63], v[32:35]
	v_mfma_f32_16x16x128_f8f6f4 v[230:233], v[158:165], v[56:63], v[40:43]
	v_mfma_f32_16x16x128_f8f6f4 v[238:241], v[158:165], v[80:87], v[20:23]
	v_mfma_f32_16x16x128_f8f6f4 v[242:245], v[166:173], v[80:87], v[16:19]
	v_mfma_f32_16x16x128_f8f6f4 v[250:253], v[166:173], v[88:95], v[0:3]
	v_mfma_f32_16x16x128_f8f6f4 v[246:249], v[158:165], v[88:95], v[4:7]
	s_barrier
	s_nop 4
	ds_read_b128 v[0:3], v156
	ds_read_b128 v[4:7], v156 offset:1024
	ds_read_b128 v[16:19], v156 offset:2048
	ds_read_b128 v[20:23], v156 offset:3072
	ds_read_b128 v[132:135], v157
	ds_read_b128 v[136:139], v157 offset:1024
	ds_read_b128 v[140:143], v157 offset:2048
	ds_read_b128 v[144:147], v157 offset:3072
	ds_read_b128 v[8:11], v155 offset:32768
	ds_read_b128 v[12:15], v155 offset:33792
	ds_read_b128 v[24:27], v155 offset:34816
	ds_read_b128 v[28:31], v155 offset:35840
	ds_read_b128 v[32:35], v155 offset:36864
	ds_read_b128 v[36:39], v155 offset:37888
	ds_read_b128 v[40:43], v155 offset:38912
	ds_read_b128 v[44:47], v155 offset:39936
	s_add_u32 s26, s36, 0xe0000
	s_addc_u32 s27, s37, 0
	s_add_i32 m0, s44, 0x4000
	s_nop 0
	global_load_lds_dwordx4 v149, s[26:27]
	s_add_i32 m0, s44, 0x6000
	s_nop 0
	global_load_lds_dwordx4 v151, s[26:27]
	s_waitcnt vmcnt(8) lgkmcnt(0)
	s_barrier
	v_mfma_f32_16x16x128_f8f6f4 v[112:115], v[0:7], v[8:15], v[112:115]
	v_mfma_f32_16x16x128_f8f6f4 v[116:119], v[16:23], v[8:15], v[116:119]
	v_mfma_f32_16x16x128_f8f6f4 v[96:99], v[16:23], v[24:31], v[96:99]
	v_mfma_f32_16x16x128_f8f6f4 v[100:103], v[0:7], v[24:31], v[100:103]
	v_mfma_f32_16x16x128_f8f6f4 v[84:87], v[0:7], v[32:39], v[206:209]
	v_mfma_f32_16x16x128_f8f6f4 v[80:83], v[16:23], v[32:39], v[210:213]
	v_mfma_f32_16x16x128_f8f6f4 v[52:55], v[16:23], v[40:47], v[218:221]
	v_mfma_f32_16x16x128_f8f6f4 v[60:63], v[0:7], v[40:47], v[214:217]
	v_mfma_f32_16x16x128_f8f6f4 v[120:123], v[132:139], v[8:15], v[120:123]
	v_mfma_f32_16x16x128_f8f6f4 v[124:127], v[140:147], v[8:15], v[124:127]
	v_mfma_f32_16x16x128_f8f6f4 v[104:107], v[140:147], v[24:31], v[104:107]
	v_mfma_f32_16x16x128_f8f6f4 v[108:111], v[132:139], v[24:31], v[108:111]
	v_mfma_f32_16x16x128_f8f6f4 v[92:95], v[132:139], v[32:39], v[174:177]
	v_mfma_f32_16x16x128_f8f6f4 v[88:91], v[140:147], v[32:39], v[178:181]
	v_mfma_f32_16x16x128_f8f6f4 v[48:51], v[140:147], v[40:47], v[186:189]
	v_mfma_f32_16x16x128_f8f6f4 v[56:59], v[132:139], v[40:47], v[182:185]
	s_barrier
	ds_read_b128 v[158:161], v155 offset:49152
	ds_read_b128 v[162:165], v155 offset:50176
	ds_read_b128 v[166:169], v155 offset:51200
	ds_read_b128 v[170:173], v155 offset:52224
	ds_read_b128 v[174:177], v155 offset:53248
	ds_read_b128 v[178:181], v155 offset:54272
	ds_read_b128 v[182:185], v155 offset:55296
	ds_read_b128 v[186:189], v155 offset:56320
	s_add_i32 m0, s44, 0x18000
	s_nop 0
	global_load_lds_dwordx4 v150, s[34:35]
	s_add_i32 m0, s44, 0x1a000
	s_nop 0
	global_load_lds_dwordx4 v152, s[34:35]
	s_add_u32 s26, s30, 0xe0080
	s_addc_u32 s27, s31, 0
	s_add_i32 m0, s44, 0x1c000
	s_nop 0
	global_load_lds_dwordx4 v150, s[26:27]
	s_add_i32 m0, s44, 0x1e000
	s_nop 0
	global_load_lds_dwordx4 v152, s[26:27]
	s_add_i32 m0, s44, 0x8000
	s_nop 0
	global_load_lds_dwordx4 v149, s[28:29]
	s_add_i32 m0, s44, 0xa000
	s_nop 0
	global_load_lds_dwordx4 v151, s[28:29]
	s_add_i32 s52, s52, 2
	s_add_u32 s23, s23, 0x100
	s_addc_u32 s51, s51, 0
	s_cmp_gt_u32 s52, 53
	s_mov_b64 s[26:27], s[24:25]
	s_waitcnt vmcnt(8) lgkmcnt(0)
	s_barrier
	v_mfma_f32_16x16x128_f8f6f4 v[68:71], v[0:7], v[158:165], v[68:71]
	v_mfma_f32_16x16x128_f8f6f4 v[64:67], v[16:23], v[158:165], v[64:67]
	v_mfma_f32_16x16x128_f8f6f4 v[36:39], v[16:23], v[166:173], v[194:197]
	v_mfma_f32_16x16x128_f8f6f4 v[44:47], v[0:7], v[166:173], v[190:193]
	v_mfma_f32_16x16x128_f8f6f4 v[28:31], v[0:7], v[174:181], v[198:201]
	v_mfma_f32_16x16x128_f8f6f4 v[24:27], v[16:23], v[174:181], v[202:205]
	v_mfma_f32_16x16x128_f8f6f4 v[8:11], v[16:23], v[182:189], v[226:229]
	v_mfma_f32_16x16x128_f8f6f4 v[12:15], v[0:7], v[182:189], v[222:225]
	v_mfma_f32_16x16x128_f8f6f4 v[76:79], v[132:139], v[158:165], v[76:79]
	v_mfma_f32_16x16x128_f8f6f4 v[72:75], v[140:147], v[158:165], v[72:75]
	v_mfma_f32_16x16x128_f8f6f4 v[32:35], v[140:147], v[166:173], v[234:237]
	v_mfma_f32_16x16x128_f8f6f4 v[40:43], v[132:139], v[166:173], v[230:233]
	v_mfma_f32_16x16x128_f8f6f4 v[20:23], v[132:139], v[174:181], v[238:241]
	v_mfma_f32_16x16x128_f8f6f4 v[16:19], v[140:147], v[174:181], v[242:245]
	v_mfma_f32_16x16x128_f8f6f4 v[0:3], v[140:147], v[182:189], v[250:253]
	v_mfma_f32_16x16x128_f8f6f4 v[4:7], v[132:139], v[182:189], v[246:249]
	s_barrier
	s_cbranch_scc0 .LBB0_1488
	s_and_b64 vcc, exec, s[16:17]
	s_cbranch_vccz .LBB0_1491
	s_barrier
